# scale load first + exit granularity 2 + late W barrier on top of the ring-4 in-loop-scale layers
# speedup vs baseline: 1.0148x; 1.0137x over previous
.Lg1_active:
	s_mov_b32 s46, 0x01010101
	s_mov_b32 s47, 0x01010101
	s_mov_b32 s60, 0x00ff00ff
	s_mov_b32 s61, 0x0c030c01
	v_lshrrev_b32_e32 v107, 3, v1
	v_and_b32_e32 v108, 7, v1
	v_and_b32_e32 v105, 15, v1
	v_lshrrev_b32_e32 v106, 4, v1
	s_bfe_u32 s36, s3, 0x10002
	s_lshl_b32 s58, s36, 3
	s_xor_b32 s59, s58, 8
	v_or_b32_e32 v102, s58, v107
	v_or_b32_e32 v103, s59, v107
	v_lshlrev_b32_e32 v89, 4, v108
	v_and_b32_e32 v90, 56, v1
	v_lshlrev_b32_e32 v90, 2, v90
	s_waitcnt lgkmcnt(0)
	s_lshl_b32 s58, s6, 8
	s_add_u32 s32, s16, s58
	s_addc_u32 s33, s17, 0
	s_lshl_b32 s58, s6, 10
	s_add_u32 s34, s18, s58
	s_addc_u32 s35, s19, 0
	v_lshlrev_b32_e32 v109, 4, v105
	global_load_dword v104, v109, s[32:33] offset:8
	v_lshlrev_b32_e32 v110, 4, v102
	global_load_dwordx2 v[68:69], v110, s[32:33]
	v_lshlrev_b32_e32 v111, 4, v103
	global_load_dwordx2 v[70:71], v111, s[32:33]
	v_lshlrev_b32_e32 v101, 2, v108
	v_lshl_or_b32 v110, v102, 6, v101
	global_load_dword v60, v110, s[34:35]
	global_load_dword v61, v110, s[34:35] offset:32
	v_lshl_or_b32 v111, v103, 6, v101
	global_load_dword v62, v111, s[34:35]
	global_load_dword v63, v111, s[34:35] offset:32
	global_load_dwordx4 v[2:5], v95, s[22:23]
	global_load_dwordx4 v[6:9], v98, s[22:23]
	global_load_dwordx4 v[10:13], v99, s[22:23]
	global_load_dwordx4 v[14:17], v100, s[22:23]
	v_and_b32_e32 v101, 0x7f, v0
	v_lshlrev_b32_e32 v101, 2, v101
	global_load_dword v19, v101, s[24:25]
	s_mul_i32 s48, s3, 0x1100
	s_add_u32 s48, s48, 66048
	v_mul_u32_u24_e32 v91, 0x110, v102
	v_lshl_add_u32 v91, v108, 5, v91
	v_add_u32_e32 v91, s48, v91
	v_mul_u32_u24_e32 v92, 0x110, v103
	v_lshl_add_u32 v92, v108, 5, v92
	v_add_u32_e32 v92, s48, v92
	s_waitcnt vmcnt(5)
	v_readlane_b32 s49, v69, 0
	v_readlane_b32 s50, v69, 8
	v_readlane_b32 s51, v69, 16
	v_readlane_b32 s52, v69, 24
	v_readlane_b32 s53, v69, 32
	v_readlane_b32 s54, v69, 40
	v_readlane_b32 s55, v69, 48
	v_readlane_b32 s56, v69, 56
	s_max_i32 s37, s49, s50
	s_max_i32 s37, s37, s51
	s_max_i32 s37, s37, s52
	s_max_i32 s37, s37, s53
	s_max_i32 s37, s37, s54
	s_max_i32 s37, s37, s55
	s_max_i32 s37, s37, s56
	v_readlane_b32 s49, v71, 0
	v_readlane_b32 s50, v71, 8
	v_readlane_b32 s51, v71, 16
	v_readlane_b32 s52, v71, 24
	v_readlane_b32 s53, v71, 32
	v_readlane_b32 s54, v71, 40
	v_readlane_b32 s55, v71, 48
	v_readlane_b32 s56, v71, 56
	s_max_i32 s38, s49, s50
	s_max_i32 s38, s38, s51
	s_max_i32 s38, s38, s52
	s_max_i32 s38, s38, s53
	s_max_i32 s38, s38, s54
	s_max_i32 s38, s38, s55
	s_max_i32 s38, s38, s56
	v_lshlrev_b32_e32 v103, 9, v104
	v_lshl_or_b32 v103, v106, 5, v103
	s_waitcnt vmcnt(0)
	ds_write_b128 v96, v[2:5]
	ds_write_b128 v96, v[6:9] offset:16384
	ds_write_b128 v96, v[10:13] offset:32768
	ds_write_b128 v96, v[14:17] offset:49152
	v_add_u32_e32 v101, 0x10000, v101
	ds_write_b32 v101, v19
	s_mov_b32 s39, 0

.Lg1_sel_done:
	s_min_i32 s40, s41, 32
	s_add_i32 s40, s40, 1
	s_and_b32 s40, s40, 62
	s_max_i32 s40, s40, 4
	v_mov_b32_e32 v2, 0
	v_mov_b32_e32 v3, 0
	v_mov_b32_e32 v4, 0
	v_mov_b32_e32 v5, 0
	v_mov_b32_e32 v6, 0
	v_mov_b32_e32 v7, 0
	v_mov_b32_e32 v8, 0
	v_mov_b32_e32 v9, 0
	v_mov_b32_e32 v10, 0
	v_mov_b32_e32 v11, 0
	v_mov_b32_e32 v12, 0
	v_mov_b32_e32 v13, 0
	v_mov_b32_e32 v14, 0
	v_mov_b32_e32 v15, 0
	v_mov_b32_e32 v16, 0
	v_mov_b32_e32 v17, 0
	v_mov_b32_e32 v18, 0
	s_waitcnt lgkmcnt(0)
	ds_bpermute_b32 v94, v90, v73 offset:0
	ds_bpermute_b32 v95, v90, v73 offset:4
	ds_bpermute_b32 v79, v90, v73 offset:8
	s_waitcnt lgkmcnt(1)
	v_and_b32_e32 v84, 0xffff, v94
	v_lshlrev_b32_e32 v109, 1, v84
	v_lshl_or_b32 v83, v84, 7, v89
	global_load_ushort v52, v109, s[14:15]
	global_load_dwordx4 v[20:23], v83, s[12:13]
	v_lshrrev_b32_e32 v84, 16, v94
	v_lshlrev_b32_e32 v109, 1, v84
	v_lshl_or_b32 v83, v84, 7, v89
	global_load_ushort v53, v109, s[14:15]
	global_load_dwordx4 v[24:27], v83, s[12:13]
	v_and_b32_e32 v84, 0xffff, v95
	v_lshlrev_b32_e32 v109, 1, v84
	v_lshl_or_b32 v83, v84, 7, v89
	global_load_ushort v54, v109, s[14:15]
	global_load_dwordx4 v[28:31], v83, s[12:13]
	v_lshrrev_b32_e32 v84, 16, v95
	v_lshlrev_b32_e32 v109, 1, v84
	v_lshl_or_b32 v83, v84, 7, v89
	global_load_ushort v55, v109, s[14:15]
	global_load_dwordx4 v[32:35], v83, s[12:13]
	s_cmp_eq_u32 s39, 0
	s_cbranch_scc0 .Lg1_nobar
	s_waitcnt lgkmcnt(0)
	s_barrier
.Lg1_nobar:
	s_cmp_le_u32 s40, 4
	s_cbranch_scc1 .Lg1_tail0
	s_waitcnt lgkmcnt(0)
	ds_bpermute_b32 v80, v90, v73 offset:12
	s_waitcnt vmcnt(6)
	v_cvt_f32_f16_e32 v52, v52
	v_cvt_f32_ubyte0_e32 v85, v20
	v_cvt_f32_ubyte1_e32 v86, v20
	v_cvt_f32_ubyte2_e32 v87, v20
	v_cvt_f32_ubyte3_e32 v88, v20
	v_fmac_f32_e32 v2, v85, v52
	v_fmac_f32_e32 v3, v86, v52
	v_fmac_f32_e32 v4, v87, v52
	v_fmac_f32_e32 v5, v88, v52
	v_cvt_f32_ubyte0_e32 v85, v21
	v_cvt_f32_ubyte1_e32 v86, v21
	v_cvt_f32_ubyte2_e32 v87, v21
	v_cvt_f32_ubyte3_e32 v88, v21
	v_fmac_f32_e32 v6, v85, v52
	v_fmac_f32_e32 v7, v86, v52
	v_fmac_f32_e32 v8, v87, v52
	v_fmac_f32_e32 v9, v88, v52
	v_cvt_f32_ubyte0_e32 v85, v22
	v_cvt_f32_ubyte1_e32 v86, v22
	v_cvt_f32_ubyte2_e32 v87, v22
	v_cvt_f32_ubyte3_e32 v88, v22
	v_fmac_f32_e32 v10, v85, v52
	v_fmac_f32_e32 v11, v86, v52
	v_fmac_f32_e32 v12, v87, v52
	v_fmac_f32_e32 v13, v88, v52
	v_cvt_f32_ubyte0_e32 v85, v23
	v_cvt_f32_ubyte1_e32 v86, v23
	v_cvt_f32_ubyte2_e32 v87, v23
	v_cvt_f32_ubyte3_e32 v88, v23
	v_fmac_f32_e32 v14, v85, v52
	v_fmac_f32_e32 v15, v86, v52
	v_fmac_f32_e32 v16, v87, v52
	v_fmac_f32_e32 v17, v88, v52
	v_add_f32_e32 v18, v18, v52
	v_and_b32_e32 v84, 0xffff, v79
	v_lshlrev_b32_e32 v109, 1, v84
	v_lshl_or_b32 v83, v84, 7, v89
	global_load_ushort v52, v109, s[14:15]
	global_load_dwordx4 v[20:23], v83, s[12:13]
	s_waitcnt vmcnt(6)
	v_cvt_f32_f16_e32 v53, v53
	v_cvt_f32_ubyte0_e32 v85, v24
	v_cvt_f32_ubyte1_e32 v86, v24
	v_cvt_f32_ubyte2_e32 v87, v24
	v_cvt_f32_ubyte3_e32 v88, v24
	v_fmac_f32_e32 v2, v85, v53
	v_fmac_f32_e32 v3, v86, v53
	v_fmac_f32_e32 v4, v87, v53
	v_fmac_f32_e32 v5, v88, v53
	v_cvt_f32_ubyte0_e32 v85, v25
	v_cvt_f32_ubyte1_e32 v86, v25
	v_cvt_f32_ubyte2_e32 v87, v25
	v_cvt_f32_ubyte3_e32 v88, v25
	v_fmac_f32_e32 v6, v85, v53
	v_fmac_f32_e32 v7, v86, v53
	v_fmac_f32_e32 v8, v87, v53
	v_fmac_f32_e32 v9, v88, v53
	v_cvt_f32_ubyte0_e32 v85, v26
	v_cvt_f32_ubyte1_e32 v86, v26
	v_cvt_f32_ubyte2_e32 v87, v26
	v_cvt_f32_ubyte3_e32 v88, v26
	v_fmac_f32_e32 v10, v85, v53
	v_fmac_f32_e32 v11, v86, v53
	v_fmac_f32_e32 v12, v87, v53
	v_fmac_f32_e32 v13, v88, v53
	v_cvt_f32_ubyte0_e32 v85, v27
	v_cvt_f32_ubyte1_e32 v86, v27
	v_cvt_f32_ubyte2_e32 v87, v27
	v_cvt_f32_ubyte3_e32 v88, v27
	v_fmac_f32_e32 v14, v85, v53
	v_fmac_f32_e32 v15, v86, v53
	v_fmac_f32_e32 v16, v87, v53
	v_fmac_f32_e32 v17, v88, v53
	v_add_f32_e32 v18, v18, v53
	v_lshrrev_b32_e32 v84, 16, v79
	v_lshlrev_b32_e32 v109, 1, v84
	v_lshl_or_b32 v83, v84, 7, v89
	global_load_ushort v53, v109, s[14:15]
	global_load_dwordx4 v[24:27], v83, s[12:13]
	s_cmp_le_u32 s40, 6
	s_cbranch_scc1 .Lg1_tail2
	s_waitcnt lgkmcnt(0)
	ds_bpermute_b32 v79, v90, v73 offset:16
	s_waitcnt vmcnt(6)
	v_cvt_f32_f16_e32 v54, v54
	v_cvt_f32_ubyte0_e32 v85, v28
	v_cvt_f32_ubyte1_e32 v86, v28
	v_cvt_f32_ubyte2_e32 v87, v28
	v_cvt_f32_ubyte3_e32 v88, v28
	v_fmac_f32_e32 v2, v85, v54
	v_fmac_f32_e32 v3, v86, v54
	v_fmac_f32_e32 v4, v87, v54
	v_fmac_f32_e32 v5, v88, v54
	v_cvt_f32_ubyte0_e32 v85, v29
	v_cvt_f32_ubyte1_e32 v86, v29
	v_cvt_f32_ubyte2_e32 v87, v29
	v_cvt_f32_ubyte3_e32 v88, v29
	v_fmac_f32_e32 v6, v85, v54
	v_fmac_f32_e32 v7, v86, v54
	v_fmac_f32_e32 v8, v87, v54
	v_fmac_f32_e32 v9, v88, v54
	v_cvt_f32_ubyte0_e32 v85, v30
	v_cvt_f32_ubyte1_e32 v86, v30
	v_cvt_f32_ubyte2_e32 v87, v30
	v_cvt_f32_ubyte3_e32 v88, v30
	v_fmac_f32_e32 v10, v85, v54
	v_fmac_f32_e32 v11, v86, v54
	v_fmac_f32_e32 v12, v87, v54
	v_fmac_f32_e32 v13, v88, v54
	v_cvt_f32_ubyte0_e32 v85, v31
	v_cvt_f32_ubyte1_e32 v86, v31
	v_cvt_f32_ubyte2_e32 v87, v31
	v_cvt_f32_ubyte3_e32 v88, v31
	v_fmac_f32_e32 v14, v85, v54
	v_fmac_f32_e32 v15, v86, v54
	v_fmac_f32_e32 v16, v87, v54
	v_fmac_f32_e32 v17, v88, v54
	v_add_f32_e32 v18, v18, v54
	v_and_b32_e32 v84, 0xffff, v80
	v_lshlrev_b32_e32 v109, 1, v84
	v_lshl_or_b32 v83, v84, 7, v89
	global_load_ushort v54, v109, s[14:15]
	global_load_dwordx4 v[28:31], v83, s[12:13]
	s_waitcnt vmcnt(6)
	v_cvt_f32_f16_e32 v55, v55
	v_cvt_f32_ubyte0_e32 v85, v32
	v_cvt_f32_ubyte1_e32 v86, v32
	v_cvt_f32_ubyte2_e32 v87, v32
	v_cvt_f32_ubyte3_e32 v88, v32
	v_fmac_f32_e32 v2, v85, v55
	v_fmac_f32_e32 v3, v86, v55
	v_fmac_f32_e32 v4, v87, v55
	v_fmac_f32_e32 v5, v88, v55
	v_cvt_f32_ubyte0_e32 v85, v33
	v_cvt_f32_ubyte1_e32 v86, v33
	v_cvt_f32_ubyte2_e32 v87, v33
	v_cvt_f32_ubyte3_e32 v88, v33
	v_fmac_f32_e32 v6, v85, v55
	v_fmac_f32_e32 v7, v86, v55
	v_fmac_f32_e32 v8, v87, v55
	v_fmac_f32_e32 v9, v88, v55
	v_cvt_f32_ubyte0_e32 v85, v34
	v_cvt_f32_ubyte1_e32 v86, v34
	v_cvt_f32_ubyte2_e32 v87, v34
	v_cvt_f32_ubyte3_e32 v88, v34
	v_fmac_f32_e32 v10, v85, v55
	v_fmac_f32_e32 v11, v86, v55
	v_fmac_f32_e32 v12, v87, v55
	v_fmac_f32_e32 v13, v88, v55
	v_cvt_f32_ubyte0_e32 v85, v35
	v_cvt_f32_ubyte1_e32 v86, v35
	v_cvt_f32_ubyte2_e32 v87, v35
	v_cvt_f32_ubyte3_e32 v88, v35
	v_fmac_f32_e32 v14, v85, v55
	v_fmac_f32_e32 v15, v86, v55
	v_fmac_f32_e32 v16, v87, v55
	v_fmac_f32_e32 v17, v88, v55
	v_add_f32_e32 v18, v18, v55
	v_lshrrev_b32_e32 v84, 16, v80
	v_lshlrev_b32_e32 v109, 1, v84
	v_lshl_or_b32 v83, v84, 7, v89
	global_load_ushort v55, v109, s[14:15]
	global_load_dwordx4 v[32:35], v83, s[12:13]
	s_cmp_le_u32 s40, 8
	s_cbranch_scc1 .Lg1_tail0
	s_waitcnt lgkmcnt(0)
	ds_bpermute_b32 v80, v90, v73 offset:20
	s_waitcnt vmcnt(6)
	v_cvt_f32_f16_e32 v52, v52
	v_cvt_f32_ubyte0_e32 v85, v20
	v_cvt_f32_ubyte1_e32 v86, v20
	v_cvt_f32_ubyte2_e32 v87, v20
	v_cvt_f32_ubyte3_e32 v88, v20
	v_fmac_f32_e32 v2, v85, v52
	v_fmac_f32_e32 v3, v86, v52
	v_fmac_f32_e32 v4, v87, v52
	v_fmac_f32_e32 v5, v88, v52
	v_cvt_f32_ubyte0_e32 v85, v21
	v_cvt_f32_ubyte1_e32 v86, v21
	v_cvt_f32_ubyte2_e32 v87, v21
	v_cvt_f32_ubyte3_e32 v88, v21
	v_fmac_f32_e32 v6, v85, v52
	v_fmac_f32_e32 v7, v86, v52
	v_fmac_f32_e32 v8, v87, v52
	v_fmac_f32_e32 v9, v88, v52
	v_cvt_f32_ubyte0_e32 v85, v22
	v_cvt_f32_ubyte1_e32 v86, v22
	v_cvt_f32_ubyte2_e32 v87, v22
	v_cvt_f32_ubyte3_e32 v88, v22
	v_fmac_f32_e32 v10, v85, v52
	v_fmac_f32_e32 v11, v86, v52
	v_fmac_f32_e32 v12, v87, v52
	v_fmac_f32_e32 v13, v88, v52
	v_cvt_f32_ubyte0_e32 v85, v23
	v_cvt_f32_ubyte1_e32 v86, v23
	v_cvt_f32_ubyte2_e32 v87, v23
	v_cvt_f32_ubyte3_e32 v88, v23
	v_fmac_f32_e32 v14, v85, v52
	v_fmac_f32_e32 v15, v86, v52
	v_fmac_f32_e32 v16, v87, v52
	v_fmac_f32_e32 v17, v88, v52
	v_add_f32_e32 v18, v18, v52
	v_and_b32_e32 v84, 0xffff, v79
	v_lshlrev_b32_e32 v109, 1, v84
	v_lshl_or_b32 v83, v84, 7, v89
	global_load_ushort v52, v109, s[14:15]
	global_load_dwordx4 v[20:23], v83, s[12:13]
	s_waitcnt vmcnt(6)
	v_cvt_f32_f16_e32 v53, v53
	v_cvt_f32_ubyte0_e32 v85, v24
	v_cvt_f32_ubyte1_e32 v86, v24
	v_cvt_f32_ubyte2_e32 v87, v24
	v_cvt_f32_ubyte3_e32 v88, v24
	v_fmac_f32_e32 v2, v85, v53
	v_fmac_f32_e32 v3, v86, v53
	v_fmac_f32_e32 v4, v87, v53
	v_fmac_f32_e32 v5, v88, v53
	v_cvt_f32_ubyte0_e32 v85, v25
	v_cvt_f32_ubyte1_e32 v86, v25
	v_cvt_f32_ubyte2_e32 v87, v25
	v_cvt_f32_ubyte3_e32 v88, v25
	v_fmac_f32_e32 v6, v85, v53
	v_fmac_f32_e32 v7, v86, v53
	v_fmac_f32_e32 v8, v87, v53
	v_fmac_f32_e32 v9, v88, v53
	v_cvt_f32_ubyte0_e32 v85, v26
	v_cvt_f32_ubyte1_e32 v86, v26
	v_cvt_f32_ubyte2_e32 v87, v26
	v_cvt_f32_ubyte3_e32 v88, v26
	v_fmac_f32_e32 v10, v85, v53
	v_fmac_f32_e32 v11, v86, v53
	v_fmac_f32_e32 v12, v87, v53
	v_fmac_f32_e32 v13, v88, v53
	v_cvt_f32_ubyte0_e32 v85, v27
	v_cvt_f32_ubyte1_e32 v86, v27
	v_cvt_f32_ubyte2_e32 v87, v27
	v_cvt_f32_ubyte3_e32 v88, v27
	v_fmac_f32_e32 v14, v85, v53
	v_fmac_f32_e32 v15, v86, v53
	v_fmac_f32_e32 v16, v87, v53
	v_fmac_f32_e32 v17, v88, v53
	v_add_f32_e32 v18, v18, v53
	v_lshrrev_b32_e32 v84, 16, v79
	v_lshlrev_b32_e32 v109, 1, v84
	v_lshl_or_b32 v83, v84, 7, v89
	global_load_ushort v53, v109, s[14:15]
	global_load_dwordx4 v[24:27], v83, s[12:13]
	s_cmp_le_u32 s40, 10
	s_cbranch_scc1 .Lg1_tail2
	s_waitcnt lgkmcnt(0)
	ds_bpermute_b32 v79, v90, v73 offset:24
	s_waitcnt vmcnt(6)
	v_cvt_f32_f16_e32 v54, v54
	v_cvt_f32_ubyte0_e32 v85, v28
	v_cvt_f32_ubyte1_e32 v86, v28
	v_cvt_f32_ubyte2_e32 v87, v28
	v_cvt_f32_ubyte3_e32 v88, v28
	v_fmac_f32_e32 v2, v85, v54
	v_fmac_f32_e32 v3, v86, v54
	v_fmac_f32_e32 v4, v87, v54
	v_fmac_f32_e32 v5, v88, v54
	v_cvt_f32_ubyte0_e32 v85, v29
	v_cvt_f32_ubyte1_e32 v86, v29
	v_cvt_f32_ubyte2_e32 v87, v29
	v_cvt_f32_ubyte3_e32 v88, v29
	v_fmac_f32_e32 v6, v85, v54
	v_fmac_f32_e32 v7, v86, v54
	v_fmac_f32_e32 v8, v87, v54
	v_fmac_f32_e32 v9, v88, v54
	v_cvt_f32_ubyte0_e32 v85, v30
	v_cvt_f32_ubyte1_e32 v86, v30
	v_cvt_f32_ubyte2_e32 v87, v30
	v_cvt_f32_ubyte3_e32 v88, v30
	v_fmac_f32_e32 v10, v85, v54
	v_fmac_f32_e32 v11, v86, v54
	v_fmac_f32_e32 v12, v87, v54
	v_fmac_f32_e32 v13, v88, v54
	v_cvt_f32_ubyte0_e32 v85, v31
	v_cvt_f32_ubyte1_e32 v86, v31
	v_cvt_f32_ubyte2_e32 v87, v31
	v_cvt_f32_ubyte3_e32 v88, v31
	v_fmac_f32_e32 v14, v85, v54
	v_fmac_f32_e32 v15, v86, v54
	v_fmac_f32_e32 v16, v87, v54
	v_fmac_f32_e32 v17, v88, v54
	v_add_f32_e32 v18, v18, v54
	v_and_b32_e32 v84, 0xffff, v80
	v_lshlrev_b32_e32 v109, 1, v84
	v_lshl_or_b32 v83, v84, 7, v89
	global_load_ushort v54, v109, s[14:15]
	global_load_dwordx4 v[28:31], v83, s[12:13]
	s_waitcnt vmcnt(6)
	v_cvt_f32_f16_e32 v55, v55
	v_cvt_f32_ubyte0_e32 v85, v32
	v_cvt_f32_ubyte1_e32 v86, v32
	v_cvt_f32_ubyte2_e32 v87, v32
	v_cvt_f32_ubyte3_e32 v88, v32
	v_fmac_f32_e32 v2, v85, v55
	v_fmac_f32_e32 v3, v86, v55
	v_fmac_f32_e32 v4, v87, v55
	v_fmac_f32_e32 v5, v88, v55
	v_cvt_f32_ubyte0_e32 v85, v33
	v_cvt_f32_ubyte1_e32 v86, v33
	v_cvt_f32_ubyte2_e32 v87, v33
	v_cvt_f32_ubyte3_e32 v88, v33
	v_fmac_f32_e32 v6, v85, v55
	v_fmac_f32_e32 v7, v86, v55
	v_fmac_f32_e32 v8, v87, v55
	v_fmac_f32_e32 v9, v88, v55
	v_cvt_f32_ubyte0_e32 v85, v34
	v_cvt_f32_ubyte1_e32 v86, v34
	v_cvt_f32_ubyte2_e32 v87, v34
	v_cvt_f32_ubyte3_e32 v88, v34
	v_fmac_f32_e32 v10, v85, v55
	v_fmac_f32_e32 v11, v86, v55
	v_fmac_f32_e32 v12, v87, v55
	v_fmac_f32_e32 v13, v88, v55
	v_cvt_f32_ubyte0_e32 v85, v35
	v_cvt_f32_ubyte1_e32 v86, v35
	v_cvt_f32_ubyte2_e32 v87, v35
	v_cvt_f32_ubyte3_e32 v88, v35
	v_fmac_f32_e32 v14, v85, v55
	v_fmac_f32_e32 v15, v86, v55
	v_fmac_f32_e32 v16, v87, v55
	v_fmac_f32_e32 v17, v88, v55
	v_add_f32_e32 v18, v18, v55
	v_lshrrev_b32_e32 v84, 16, v80
	v_lshlrev_b32_e32 v109, 1, v84
	v_lshl_or_b32 v83, v84, 7, v89
	global_load_ushort v55, v109, s[14:15]
	global_load_dwordx4 v[32:35], v83, s[12:13]
	s_cmp_le_u32 s40, 12
	s_cbranch_scc1 .Lg1_tail0
	s_waitcnt lgkmcnt(0)
	ds_bpermute_b32 v80, v90, v73 offset:28
	s_waitcnt vmcnt(6)
	v_cvt_f32_f16_e32 v52, v52
	v_cvt_f32_ubyte0_e32 v85, v20
	v_cvt_f32_ubyte1_e32 v86, v20
	v_cvt_f32_ubyte2_e32 v87, v20
	v_cvt_f32_ubyte3_e32 v88, v20
	v_fmac_f32_e32 v2, v85, v52
	v_fmac_f32_e32 v3, v86, v52
	v_fmac_f32_e32 v4, v87, v52
	v_fmac_f32_e32 v5, v88, v52
	v_cvt_f32_ubyte0_e32 v85, v21
	v_cvt_f32_ubyte1_e32 v86, v21
	v_cvt_f32_ubyte2_e32 v87, v21
	v_cvt_f32_ubyte3_e32 v88, v21
	v_fmac_f32_e32 v6, v85, v52
	v_fmac_f32_e32 v7, v86, v52
	v_fmac_f32_e32 v8, v87, v52
	v_fmac_f32_e32 v9, v88, v52
	v_cvt_f32_ubyte0_e32 v85, v22
	v_cvt_f32_ubyte1_e32 v86, v22
	v_cvt_f32_ubyte2_e32 v87, v22
	v_cvt_f32_ubyte3_e32 v88, v22
	v_fmac_f32_e32 v10, v85, v52
	v_fmac_f32_e32 v11, v86, v52
	v_fmac_f32_e32 v12, v87, v52
	v_fmac_f32_e32 v13, v88, v52
	v_cvt_f32_ubyte0_e32 v85, v23
	v_cvt_f32_ubyte1_e32 v86, v23
	v_cvt_f32_ubyte2_e32 v87, v23
	v_cvt_f32_ubyte3_e32 v88, v23
	v_fmac_f32_e32 v14, v85, v52
	v_fmac_f32_e32 v15, v86, v52
	v_fmac_f32_e32 v16, v87, v52
	v_fmac_f32_e32 v17, v88, v52
	v_add_f32_e32 v18, v18, v52
	v_and_b32_e32 v84, 0xffff, v79
	v_lshlrev_b32_e32 v109, 1, v84
	v_lshl_or_b32 v83, v84, 7, v89
	global_load_ushort v52, v109, s[14:15]
	global_load_dwordx4 v[20:23], v83, s[12:13]
	s_waitcnt vmcnt(6)
	v_cvt_f32_f16_e32 v53, v53
	v_cvt_f32_ubyte0_e32 v85, v24
	v_cvt_f32_ubyte1_e32 v86, v24
	v_cvt_f32_ubyte2_e32 v87, v24
	v_cvt_f32_ubyte3_e32 v88, v24
	v_fmac_f32_e32 v2, v85, v53
	v_fmac_f32_e32 v3, v86, v53
	v_fmac_f32_e32 v4, v87, v53
	v_fmac_f32_e32 v5, v88, v53
	v_cvt_f32_ubyte0_e32 v85, v25
	v_cvt_f32_ubyte1_e32 v86, v25
	v_cvt_f32_ubyte2_e32 v87, v25
	v_cvt_f32_ubyte3_e32 v88, v25
	v_fmac_f32_e32 v6, v85, v53
	v_fmac_f32_e32 v7, v86, v53
	v_fmac_f32_e32 v8, v87, v53
	v_fmac_f32_e32 v9, v88, v53
	v_cvt_f32_ubyte0_e32 v85, v26
	v_cvt_f32_ubyte1_e32 v86, v26
	v_cvt_f32_ubyte2_e32 v87, v26
	v_cvt_f32_ubyte3_e32 v88, v26
	v_fmac_f32_e32 v10, v85, v53
	v_fmac_f32_e32 v11, v86, v53
	v_fmac_f32_e32 v12, v87, v53
	v_fmac_f32_e32 v13, v88, v53
	v_cvt_f32_ubyte0_e32 v85, v27
	v_cvt_f32_ubyte1_e32 v86, v27
	v_cvt_f32_ubyte2_e32 v87, v27
	v_cvt_f32_ubyte3_e32 v88, v27
	v_fmac_f32_e32 v14, v85, v53
	v_fmac_f32_e32 v15, v86, v53
	v_fmac_f32_e32 v16, v87, v53
	v_fmac_f32_e32 v17, v88, v53
	v_add_f32_e32 v18, v18, v53
	v_lshrrev_b32_e32 v84, 16, v79
	v_lshlrev_b32_e32 v109, 1, v84
	v_lshl_or_b32 v83, v84, 7, v89
	global_load_ushort v53, v109, s[14:15]
	global_load_dwordx4 v[24:27], v83, s[12:13]
	s_cmp_le_u32 s40, 14
	s_cbranch_scc1 .Lg1_tail2
	s_waitcnt lgkmcnt(0)
	ds_bpermute_b32 v79, v90, v74 offset:0
	s_waitcnt vmcnt(6)
	v_cvt_f32_f16_e32 v54, v54
	v_cvt_f32_ubyte0_e32 v85, v28
	v_cvt_f32_ubyte1_e32 v86, v28
	v_cvt_f32_ubyte2_e32 v87, v28
	v_cvt_f32_ubyte3_e32 v88, v28
	v_fmac_f32_e32 v2, v85, v54
	v_fmac_f32_e32 v3, v86, v54
	v_fmac_f32_e32 v4, v87, v54
	v_fmac_f32_e32 v5, v88, v54
	v_cvt_f32_ubyte0_e32 v85, v29
	v_cvt_f32_ubyte1_e32 v86, v29
	v_cvt_f32_ubyte2_e32 v87, v29
	v_cvt_f32_ubyte3_e32 v88, v29
	v_fmac_f32_e32 v6, v85, v54
	v_fmac_f32_e32 v7, v86, v54
	v_fmac_f32_e32 v8, v87, v54
	v_fmac_f32_e32 v9, v88, v54
	v_cvt_f32_ubyte0_e32 v85, v30
	v_cvt_f32_ubyte1_e32 v86, v30
	v_cvt_f32_ubyte2_e32 v87, v30
	v_cvt_f32_ubyte3_e32 v88, v30
	v_fmac_f32_e32 v10, v85, v54
	v_fmac_f32_e32 v11, v86, v54
	v_fmac_f32_e32 v12, v87, v54
	v_fmac_f32_e32 v13, v88, v54
	v_cvt_f32_ubyte0_e32 v85, v31
	v_cvt_f32_ubyte1_e32 v86, v31
	v_cvt_f32_ubyte2_e32 v87, v31
	v_cvt_f32_ubyte3_e32 v88, v31
	v_fmac_f32_e32 v14, v85, v54
	v_fmac_f32_e32 v15, v86, v54
	v_fmac_f32_e32 v16, v87, v54
	v_fmac_f32_e32 v17, v88, v54
	v_add_f32_e32 v18, v18, v54
	v_and_b32_e32 v84, 0xffff, v80
	v_lshlrev_b32_e32 v109, 1, v84
	v_lshl_or_b32 v83, v84, 7, v89
	global_load_ushort v54, v109, s[14:15]
	global_load_dwordx4 v[28:31], v83, s[12:13]
	s_waitcnt vmcnt(6)
	v_cvt_f32_f16_e32 v55, v55
	v_cvt_f32_ubyte0_e32 v85, v32
	v_cvt_f32_ubyte1_e32 v86, v32
	v_cvt_f32_ubyte2_e32 v87, v32
	v_cvt_f32_ubyte3_e32 v88, v32
	v_fmac_f32_e32 v2, v85, v55
	v_fmac_f32_e32 v3, v86, v55
	v_fmac_f32_e32 v4, v87, v55
	v_fmac_f32_e32 v5, v88, v55
	v_cvt_f32_ubyte0_e32 v85, v33
	v_cvt_f32_ubyte1_e32 v86, v33
	v_cvt_f32_ubyte2_e32 v87, v33
	v_cvt_f32_ubyte3_e32 v88, v33
	v_fmac_f32_e32 v6, v85, v55
	v_fmac_f32_e32 v7, v86, v55
	v_fmac_f32_e32 v8, v87, v55
	v_fmac_f32_e32 v9, v88, v55
	v_cvt_f32_ubyte0_e32 v85, v34
	v_cvt_f32_ubyte1_e32 v86, v34
	v_cvt_f32_ubyte2_e32 v87, v34
	v_cvt_f32_ubyte3_e32 v88, v34
	v_fmac_f32_e32 v10, v85, v55
	v_fmac_f32_e32 v11, v86, v55
	v_fmac_f32_e32 v12, v87, v55
	v_fmac_f32_e32 v13, v88, v55
	v_cvt_f32_ubyte0_e32 v85, v35
	v_cvt_f32_ubyte1_e32 v86, v35
	v_cvt_f32_ubyte2_e32 v87, v35
	v_cvt_f32_ubyte3_e32 v88, v35
	v_fmac_f32_e32 v14, v85, v55
	v_fmac_f32_e32 v15, v86, v55
	v_fmac_f32_e32 v16, v87, v55
	v_fmac_f32_e32 v17, v88, v55
	v_add_f32_e32 v18, v18, v55
	v_lshrrev_b32_e32 v84, 16, v80
	v_lshlrev_b32_e32 v109, 1, v84
	v_lshl_or_b32 v83, v84, 7, v89
	global_load_ushort v55, v109, s[14:15]
	global_load_dwordx4 v[32:35], v83, s[12:13]
	s_cmp_le_u32 s40, 16
	s_cbranch_scc1 .Lg1_tail0
	s_waitcnt lgkmcnt(0)
	ds_bpermute_b32 v80, v90, v74 offset:4
	s_waitcnt vmcnt(6)
	v_cvt_f32_f16_e32 v52, v52
	v_cvt_f32_ubyte0_e32 v85, v20
	v_cvt_f32_ubyte1_e32 v86, v20
	v_cvt_f32_ubyte2_e32 v87, v20
	v_cvt_f32_ubyte3_e32 v88, v20
	v_fmac_f32_e32 v2, v85, v52
	v_fmac_f32_e32 v3, v86, v52
	v_fmac_f32_e32 v4, v87, v52
	v_fmac_f32_e32 v5, v88, v52
	v_cvt_f32_ubyte0_e32 v85, v21
	v_cvt_f32_ubyte1_e32 v86, v21
	v_cvt_f32_ubyte2_e32 v87, v21
	v_cvt_f32_ubyte3_e32 v88, v21
	v_fmac_f32_e32 v6, v85, v52
	v_fmac_f32_e32 v7, v86, v52
	v_fmac_f32_e32 v8, v87, v52
	v_fmac_f32_e32 v9, v88, v52
	v_cvt_f32_ubyte0_e32 v85, v22
	v_cvt_f32_ubyte1_e32 v86, v22
	v_cvt_f32_ubyte2_e32 v87, v22
	v_cvt_f32_ubyte3_e32 v88, v22
	v_fmac_f32_e32 v10, v85, v52
	v_fmac_f32_e32 v11, v86, v52
	v_fmac_f32_e32 v12, v87, v52
	v_fmac_f32_e32 v13, v88, v52
	v_cvt_f32_ubyte0_e32 v85, v23
	v_cvt_f32_ubyte1_e32 v86, v23
	v_cvt_f32_ubyte2_e32 v87, v23
	v_cvt_f32_ubyte3_e32 v88, v23
	v_fmac_f32_e32 v14, v85, v52
	v_fmac_f32_e32 v15, v86, v52
	v_fmac_f32_e32 v16, v87, v52
	v_fmac_f32_e32 v17, v88, v52
	v_add_f32_e32 v18, v18, v52
	v_and_b32_e32 v84, 0xffff, v79
	v_lshlrev_b32_e32 v109, 1, v84
	v_lshl_or_b32 v83, v84, 7, v89
	global_load_ushort v52, v109, s[14:15]
	global_load_dwordx4 v[20:23], v83, s[12:13]
	s_waitcnt vmcnt(6)
	v_cvt_f32_f16_e32 v53, v53
	v_cvt_f32_ubyte0_e32 v85, v24
	v_cvt_f32_ubyte1_e32 v86, v24
	v_cvt_f32_ubyte2_e32 v87, v24
	v_cvt_f32_ubyte3_e32 v88, v24
	v_fmac_f32_e32 v2, v85, v53
	v_fmac_f32_e32 v3, v86, v53
	v_fmac_f32_e32 v4, v87, v53
	v_fmac_f32_e32 v5, v88, v53
	v_cvt_f32_ubyte0_e32 v85, v25
	v_cvt_f32_ubyte1_e32 v86, v25
	v_cvt_f32_ubyte2_e32 v87, v25
	v_cvt_f32_ubyte3_e32 v88, v25
	v_fmac_f32_e32 v6, v85, v53
	v_fmac_f32_e32 v7, v86, v53
	v_fmac_f32_e32 v8, v87, v53
	v_fmac_f32_e32 v9, v88, v53
	v_cvt_f32_ubyte0_e32 v85, v26
	v_cvt_f32_ubyte1_e32 v86, v26
	v_cvt_f32_ubyte2_e32 v87, v26
	v_cvt_f32_ubyte3_e32 v88, v26
	v_fmac_f32_e32 v10, v85, v53
	v_fmac_f32_e32 v11, v86, v53
	v_fmac_f32_e32 v12, v87, v53
	v_fmac_f32_e32 v13, v88, v53
	v_cvt_f32_ubyte0_e32 v85, v27
	v_cvt_f32_ubyte1_e32 v86, v27
	v_cvt_f32_ubyte2_e32 v87, v27
	v_cvt_f32_ubyte3_e32 v88, v27
	v_fmac_f32_e32 v14, v85, v53
	v_fmac_f32_e32 v15, v86, v53
	v_fmac_f32_e32 v16, v87, v53
	v_fmac_f32_e32 v17, v88, v53
	v_add_f32_e32 v18, v18, v53
	v_lshrrev_b32_e32 v84, 16, v79
	v_lshlrev_b32_e32 v109, 1, v84
	v_lshl_or_b32 v83, v84, 7, v89
	global_load_ushort v53, v109, s[14:15]
	global_load_dwordx4 v[24:27], v83, s[12:13]
	s_cmp_le_u32 s40, 18
	s_cbranch_scc1 .Lg1_tail2
	s_waitcnt lgkmcnt(0)
	ds_bpermute_b32 v79, v90, v74 offset:8
	s_waitcnt vmcnt(6)
	v_cvt_f32_f16_e32 v54, v54
	v_cvt_f32_ubyte0_e32 v85, v28
	v_cvt_f32_ubyte1_e32 v86, v28
	v_cvt_f32_ubyte2_e32 v87, v28
	v_cvt_f32_ubyte3_e32 v88, v28
	v_fmac_f32_e32 v2, v85, v54
	v_fmac_f32_e32 v3, v86, v54
	v_fmac_f32_e32 v4, v87, v54
	v_fmac_f32_e32 v5, v88, v54
	v_cvt_f32_ubyte0_e32 v85, v29
	v_cvt_f32_ubyte1_e32 v86, v29
	v_cvt_f32_ubyte2_e32 v87, v29
	v_cvt_f32_ubyte3_e32 v88, v29
	v_fmac_f32_e32 v6, v85, v54
	v_fmac_f32_e32 v7, v86, v54
	v_fmac_f32_e32 v8, v87, v54
	v_fmac_f32_e32 v9, v88, v54
	v_cvt_f32_ubyte0_e32 v85, v30
	v_cvt_f32_ubyte1_e32 v86, v30
	v_cvt_f32_ubyte2_e32 v87, v30
	v_cvt_f32_ubyte3_e32 v88, v30
	v_fmac_f32_e32 v10, v85, v54
	v_fmac_f32_e32 v11, v86, v54
	v_fmac_f32_e32 v12, v87, v54
	v_fmac_f32_e32 v13, v88, v54
	v_cvt_f32_ubyte0_e32 v85, v31
	v_cvt_f32_ubyte1_e32 v86, v31
	v_cvt_f32_ubyte2_e32 v87, v31
	v_cvt_f32_ubyte3_e32 v88, v31
	v_fmac_f32_e32 v14, v85, v54
	v_fmac_f32_e32 v15, v86, v54
	v_fmac_f32_e32 v16, v87, v54
	v_fmac_f32_e32 v17, v88, v54
	v_add_f32_e32 v18, v18, v54
	v_and_b32_e32 v84, 0xffff, v80
	v_lshlrev_b32_e32 v109, 1, v84
	v_lshl_or_b32 v83, v84, 7, v89
	global_load_ushort v54, v109, s[14:15]
	global_load_dwordx4 v[28:31], v83, s[12:13]
	s_waitcnt vmcnt(6)
	v_cvt_f32_f16_e32 v55, v55
	v_cvt_f32_ubyte0_e32 v85, v32
	v_cvt_f32_ubyte1_e32 v86, v32
	v_cvt_f32_ubyte2_e32 v87, v32
	v_cvt_f32_ubyte3_e32 v88, v32
	v_fmac_f32_e32 v2, v85, v55
	v_fmac_f32_e32 v3, v86, v55
	v_fmac_f32_e32 v4, v87, v55
	v_fmac_f32_e32 v5, v88, v55
	v_cvt_f32_ubyte0_e32 v85, v33
	v_cvt_f32_ubyte1_e32 v86, v33
	v_cvt_f32_ubyte2_e32 v87, v33
	v_cvt_f32_ubyte3_e32 v88, v33
	v_fmac_f32_e32 v6, v85, v55
	v_fmac_f32_e32 v7, v86, v55
	v_fmac_f32_e32 v8, v87, v55
	v_fmac_f32_e32 v9, v88, v55
	v_cvt_f32_ubyte0_e32 v85, v34
	v_cvt_f32_ubyte1_e32 v86, v34
	v_cvt_f32_ubyte2_e32 v87, v34
	v_cvt_f32_ubyte3_e32 v88, v34
	v_fmac_f32_e32 v10, v85, v55
	v_fmac_f32_e32 v11, v86, v55
	v_fmac_f32_e32 v12, v87, v55
	v_fmac_f32_e32 v13, v88, v55
	v_cvt_f32_ubyte0_e32 v85, v35
	v_cvt_f32_ubyte1_e32 v86, v35
	v_cvt_f32_ubyte2_e32 v87, v35
	v_cvt_f32_ubyte3_e32 v88, v35
	v_fmac_f32_e32 v14, v85, v55
	v_fmac_f32_e32 v15, v86, v55
	v_fmac_f32_e32 v16, v87, v55
	v_fmac_f32_e32 v17, v88, v55
	v_add_f32_e32 v18, v18, v55
	v_lshrrev_b32_e32 v84, 16, v80
	v_lshlrev_b32_e32 v109, 1, v84
	v_lshl_or_b32 v83, v84, 7, v89
	global_load_ushort v55, v109, s[14:15]
	global_load_dwordx4 v[32:35], v83, s[12:13]
	s_cmp_le_u32 s40, 20
	s_cbranch_scc1 .Lg1_tail0
	s_waitcnt lgkmcnt(0)
	ds_bpermute_b32 v80, v90, v74 offset:12
	s_waitcnt vmcnt(6)
	v_cvt_f32_f16_e32 v52, v52
	v_cvt_f32_ubyte0_e32 v85, v20
	v_cvt_f32_ubyte1_e32 v86, v20
	v_cvt_f32_ubyte2_e32 v87, v20
	v_cvt_f32_ubyte3_e32 v88, v20
	v_fmac_f32_e32 v2, v85, v52
	v_fmac_f32_e32 v3, v86, v52
	v_fmac_f32_e32 v4, v87, v52
	v_fmac_f32_e32 v5, v88, v52
	v_cvt_f32_ubyte0_e32 v85, v21
	v_cvt_f32_ubyte1_e32 v86, v21
	v_cvt_f32_ubyte2_e32 v87, v21
	v_cvt_f32_ubyte3_e32 v88, v21
	v_fmac_f32_e32 v6, v85, v52
	v_fmac_f32_e32 v7, v86, v52
	v_fmac_f32_e32 v8, v87, v52
	v_fmac_f32_e32 v9, v88, v52
	v_cvt_f32_ubyte0_e32 v85, v22
	v_cvt_f32_ubyte1_e32 v86, v22
	v_cvt_f32_ubyte2_e32 v87, v22
	v_cvt_f32_ubyte3_e32 v88, v22
	v_fmac_f32_e32 v10, v85, v52
	v_fmac_f32_e32 v11, v86, v52
	v_fmac_f32_e32 v12, v87, v52
	v_fmac_f32_e32 v13, v88, v52
	v_cvt_f32_ubyte0_e32 v85, v23
	v_cvt_f32_ubyte1_e32 v86, v23
	v_cvt_f32_ubyte2_e32 v87, v23
	v_cvt_f32_ubyte3_e32 v88, v23
	v_fmac_f32_e32 v14, v85, v52
	v_fmac_f32_e32 v15, v86, v52
	v_fmac_f32_e32 v16, v87, v52
	v_fmac_f32_e32 v17, v88, v52
	v_add_f32_e32 v18, v18, v52
	v_and_b32_e32 v84, 0xffff, v79
	v_lshlrev_b32_e32 v109, 1, v84
	v_lshl_or_b32 v83, v84, 7, v89
	global_load_ushort v52, v109, s[14:15]
	global_load_dwordx4 v[20:23], v83, s[12:13]
	s_waitcnt vmcnt(6)
	v_cvt_f32_f16_e32 v53, v53
	v_cvt_f32_ubyte0_e32 v85, v24
	v_cvt_f32_ubyte1_e32 v86, v24
	v_cvt_f32_ubyte2_e32 v87, v24
	v_cvt_f32_ubyte3_e32 v88, v24
	v_fmac_f32_e32 v2, v85, v53
	v_fmac_f32_e32 v3, v86, v53
	v_fmac_f32_e32 v4, v87, v53
	v_fmac_f32_e32 v5, v88, v53
	v_cvt_f32_ubyte0_e32 v85, v25
	v_cvt_f32_ubyte1_e32 v86, v25
	v_cvt_f32_ubyte2_e32 v87, v25
	v_cvt_f32_ubyte3_e32 v88, v25
	v_fmac_f32_e32 v6, v85, v53
	v_fmac_f32_e32 v7, v86, v53
	v_fmac_f32_e32 v8, v87, v53
	v_fmac_f32_e32 v9, v88, v53
	v_cvt_f32_ubyte0_e32 v85, v26
	v_cvt_f32_ubyte1_e32 v86, v26
	v_cvt_f32_ubyte2_e32 v87, v26
	v_cvt_f32_ubyte3_e32 v88, v26
	v_fmac_f32_e32 v10, v85, v53
	v_fmac_f32_e32 v11, v86, v53
	v_fmac_f32_e32 v12, v87, v53
	v_fmac_f32_e32 v13, v88, v53
	v_cvt_f32_ubyte0_e32 v85, v27
	v_cvt_f32_ubyte1_e32 v86, v27
	v_cvt_f32_ubyte2_e32 v87, v27
	v_cvt_f32_ubyte3_e32 v88, v27
	v_fmac_f32_e32 v14, v85, v53
	v_fmac_f32_e32 v15, v86, v53
	v_fmac_f32_e32 v16, v87, v53
	v_fmac_f32_e32 v17, v88, v53
	v_add_f32_e32 v18, v18, v53
	v_lshrrev_b32_e32 v84, 16, v79
	v_lshlrev_b32_e32 v109, 1, v84
	v_lshl_or_b32 v83, v84, 7, v89
	global_load_ushort v53, v109, s[14:15]
	global_load_dwordx4 v[24:27], v83, s[12:13]
	s_cmp_le_u32 s40, 22
	s_cbranch_scc1 .Lg1_tail2
	s_waitcnt lgkmcnt(0)
	ds_bpermute_b32 v79, v90, v74 offset:16
	s_waitcnt vmcnt(6)
	v_cvt_f32_f16_e32 v54, v54
	v_cvt_f32_ubyte0_e32 v85, v28
	v_cvt_f32_ubyte1_e32 v86, v28
	v_cvt_f32_ubyte2_e32 v87, v28
	v_cvt_f32_ubyte3_e32 v88, v28
	v_fmac_f32_e32 v2, v85, v54
	v_fmac_f32_e32 v3, v86, v54
	v_fmac_f32_e32 v4, v87, v54
	v_fmac_f32_e32 v5, v88, v54
	v_cvt_f32_ubyte0_e32 v85, v29
	v_cvt_f32_ubyte1_e32 v86, v29
	v_cvt_f32_ubyte2_e32 v87, v29
	v_cvt_f32_ubyte3_e32 v88, v29
	v_fmac_f32_e32 v6, v85, v54
	v_fmac_f32_e32 v7, v86, v54
	v_fmac_f32_e32 v8, v87, v54
	v_fmac_f32_e32 v9, v88, v54
	v_cvt_f32_ubyte0_e32 v85, v30
	v_cvt_f32_ubyte1_e32 v86, v30
	v_cvt_f32_ubyte2_e32 v87, v30
	v_cvt_f32_ubyte3_e32 v88, v30
	v_fmac_f32_e32 v10, v85, v54
	v_fmac_f32_e32 v11, v86, v54
	v_fmac_f32_e32 v12, v87, v54
	v_fmac_f32_e32 v13, v88, v54
	v_cvt_f32_ubyte0_e32 v85, v31
	v_cvt_f32_ubyte1_e32 v86, v31
	v_cvt_f32_ubyte2_e32 v87, v31
	v_cvt_f32_ubyte3_e32 v88, v31
	v_fmac_f32_e32 v14, v85, v54
	v_fmac_f32_e32 v15, v86, v54
	v_fmac_f32_e32 v16, v87, v54
	v_fmac_f32_e32 v17, v88, v54
	v_add_f32_e32 v18, v18, v54
	v_and_b32_e32 v84, 0xffff, v80
	v_lshlrev_b32_e32 v109, 1, v84
	v_lshl_or_b32 v83, v84, 7, v89
	global_load_ushort v54, v109, s[14:15]
	global_load_dwordx4 v[28:31], v83, s[12:13]
	s_waitcnt vmcnt(6)
	v_cvt_f32_f16_e32 v55, v55
	v_cvt_f32_ubyte0_e32 v85, v32
	v_cvt_f32_ubyte1_e32 v86, v32
	v_cvt_f32_ubyte2_e32 v87, v32
	v_cvt_f32_ubyte3_e32 v88, v32
	v_fmac_f32_e32 v2, v85, v55
	v_fmac_f32_e32 v3, v86, v55
	v_fmac_f32_e32 v4, v87, v55
	v_fmac_f32_e32 v5, v88, v55
	v_cvt_f32_ubyte0_e32 v85, v33
	v_cvt_f32_ubyte1_e32 v86, v33
	v_cvt_f32_ubyte2_e32 v87, v33
	v_cvt_f32_ubyte3_e32 v88, v33
	v_fmac_f32_e32 v6, v85, v55
	v_fmac_f32_e32 v7, v86, v55
	v_fmac_f32_e32 v8, v87, v55
	v_fmac_f32_e32 v9, v88, v55
	v_cvt_f32_ubyte0_e32 v85, v34
	v_cvt_f32_ubyte1_e32 v86, v34
	v_cvt_f32_ubyte2_e32 v87, v34
	v_cvt_f32_ubyte3_e32 v88, v34
	v_fmac_f32_e32 v10, v85, v55
	v_fmac_f32_e32 v11, v86, v55
	v_fmac_f32_e32 v12, v87, v55
	v_fmac_f32_e32 v13, v88, v55
	v_cvt_f32_ubyte0_e32 v85, v35
	v_cvt_f32_ubyte1_e32 v86, v35
	v_cvt_f32_ubyte2_e32 v87, v35
	v_cvt_f32_ubyte3_e32 v88, v35
	v_fmac_f32_e32 v14, v85, v55
	v_fmac_f32_e32 v15, v86, v55
	v_fmac_f32_e32 v16, v87, v55
	v_fmac_f32_e32 v17, v88, v55
	v_add_f32_e32 v18, v18, v55
	v_lshrrev_b32_e32 v84, 16, v80
	v_lshlrev_b32_e32 v109, 1, v84
	v_lshl_or_b32 v83, v84, 7, v89
	global_load_ushort v55, v109, s[14:15]
	global_load_dwordx4 v[32:35], v83, s[12:13]
	s_cmp_le_u32 s40, 24
	s_cbranch_scc1 .Lg1_tail0
	s_waitcnt lgkmcnt(0)
	ds_bpermute_b32 v80, v90, v74 offset:20
	s_waitcnt vmcnt(6)
	v_cvt_f32_f16_e32 v52, v52
	v_cvt_f32_ubyte0_e32 v85, v20
	v_cvt_f32_ubyte1_e32 v86, v20
	v_cvt_f32_ubyte2_e32 v87, v20
	v_cvt_f32_ubyte3_e32 v88, v20
	v_fmac_f32_e32 v2, v85, v52
	v_fmac_f32_e32 v3, v86, v52
	v_fmac_f32_e32 v4, v87, v52
	v_fmac_f32_e32 v5, v88, v52
	v_cvt_f32_ubyte0_e32 v85, v21
	v_cvt_f32_ubyte1_e32 v86, v21
	v_cvt_f32_ubyte2_e32 v87, v21
	v_cvt_f32_ubyte3_e32 v88, v21
	v_fmac_f32_e32 v6, v85, v52
	v_fmac_f32_e32 v7, v86, v52
	v_fmac_f32_e32 v8, v87, v52
	v_fmac_f32_e32 v9, v88, v52
	v_cvt_f32_ubyte0_e32 v85, v22
	v_cvt_f32_ubyte1_e32 v86, v22
	v_cvt_f32_ubyte2_e32 v87, v22
	v_cvt_f32_ubyte3_e32 v88, v22
	v_fmac_f32_e32 v10, v85, v52
	v_fmac_f32_e32 v11, v86, v52
	v_fmac_f32_e32 v12, v87, v52
	v_fmac_f32_e32 v13, v88, v52
	v_cvt_f32_ubyte0_e32 v85, v23
	v_cvt_f32_ubyte1_e32 v86, v23
	v_cvt_f32_ubyte2_e32 v87, v23
	v_cvt_f32_ubyte3_e32 v88, v23
	v_fmac_f32_e32 v14, v85, v52
	v_fmac_f32_e32 v15, v86, v52
	v_fmac_f32_e32 v16, v87, v52
	v_fmac_f32_e32 v17, v88, v52
	v_add_f32_e32 v18, v18, v52
	v_and_b32_e32 v84, 0xffff, v79
	v_lshlrev_b32_e32 v109, 1, v84
	v_lshl_or_b32 v83, v84, 7, v89
	global_load_ushort v52, v109, s[14:15]
	global_load_dwordx4 v[20:23], v83, s[12:13]
	s_waitcnt vmcnt(6)
	v_cvt_f32_f16_e32 v53, v53
	v_cvt_f32_ubyte0_e32 v85, v24
	v_cvt_f32_ubyte1_e32 v86, v24
	v_cvt_f32_ubyte2_e32 v87, v24
	v_cvt_f32_ubyte3_e32 v88, v24
	v_fmac_f32_e32 v2, v85, v53
	v_fmac_f32_e32 v3, v86, v53
	v_fmac_f32_e32 v4, v87, v53
	v_fmac_f32_e32 v5, v88, v53
	v_cvt_f32_ubyte0_e32 v85, v25
	v_cvt_f32_ubyte1_e32 v86, v25
	v_cvt_f32_ubyte2_e32 v87, v25
	v_cvt_f32_ubyte3_e32 v88, v25
	v_fmac_f32_e32 v6, v85, v53
	v_fmac_f32_e32 v7, v86, v53
	v_fmac_f32_e32 v8, v87, v53
	v_fmac_f32_e32 v9, v88, v53
	v_cvt_f32_ubyte0_e32 v85, v26
	v_cvt_f32_ubyte1_e32 v86, v26
	v_cvt_f32_ubyte2_e32 v87, v26
	v_cvt_f32_ubyte3_e32 v88, v26
	v_fmac_f32_e32 v10, v85, v53
	v_fmac_f32_e32 v11, v86, v53
	v_fmac_f32_e32 v12, v87, v53
	v_fmac_f32_e32 v13, v88, v53
	v_cvt_f32_ubyte0_e32 v85, v27
	v_cvt_f32_ubyte1_e32 v86, v27
	v_cvt_f32_ubyte2_e32 v87, v27
	v_cvt_f32_ubyte3_e32 v88, v27
	v_fmac_f32_e32 v14, v85, v53
	v_fmac_f32_e32 v15, v86, v53
	v_fmac_f32_e32 v16, v87, v53
	v_fmac_f32_e32 v17, v88, v53
	v_add_f32_e32 v18, v18, v53
	v_lshrrev_b32_e32 v84, 16, v79
	v_lshlrev_b32_e32 v109, 1, v84
	v_lshl_or_b32 v83, v84, 7, v89
	global_load_ushort v53, v109, s[14:15]
	global_load_dwordx4 v[24:27], v83, s[12:13]
	s_cmp_le_u32 s40, 26
	s_cbranch_scc1 .Lg1_tail2
	s_waitcnt lgkmcnt(0)
	ds_bpermute_b32 v79, v90, v74 offset:24
	s_waitcnt vmcnt(6)
	v_cvt_f32_f16_e32 v54, v54
	v_cvt_f32_ubyte0_e32 v85, v28
	v_cvt_f32_ubyte1_e32 v86, v28
	v_cvt_f32_ubyte2_e32 v87, v28
	v_cvt_f32_ubyte3_e32 v88, v28
	v_fmac_f32_e32 v2, v85, v54
	v_fmac_f32_e32 v3, v86, v54
	v_fmac_f32_e32 v4, v87, v54
	v_fmac_f32_e32 v5, v88, v54
	v_cvt_f32_ubyte0_e32 v85, v29
	v_cvt_f32_ubyte1_e32 v86, v29
	v_cvt_f32_ubyte2_e32 v87, v29
	v_cvt_f32_ubyte3_e32 v88, v29
	v_fmac_f32_e32 v6, v85, v54
	v_fmac_f32_e32 v7, v86, v54
	v_fmac_f32_e32 v8, v87, v54
	v_fmac_f32_e32 v9, v88, v54
	v_cvt_f32_ubyte0_e32 v85, v30
	v_cvt_f32_ubyte1_e32 v86, v30
	v_cvt_f32_ubyte2_e32 v87, v30
	v_cvt_f32_ubyte3_e32 v88, v30
	v_fmac_f32_e32 v10, v85, v54
	v_fmac_f32_e32 v11, v86, v54
	v_fmac_f32_e32 v12, v87, v54
	v_fmac_f32_e32 v13, v88, v54
	v_cvt_f32_ubyte0_e32 v85, v31
	v_cvt_f32_ubyte1_e32 v86, v31
	v_cvt_f32_ubyte2_e32 v87, v31
	v_cvt_f32_ubyte3_e32 v88, v31
	v_fmac_f32_e32 v14, v85, v54
	v_fmac_f32_e32 v15, v86, v54
	v_fmac_f32_e32 v16, v87, v54
	v_fmac_f32_e32 v17, v88, v54
	v_add_f32_e32 v18, v18, v54
	v_and_b32_e32 v84, 0xffff, v80
	v_lshlrev_b32_e32 v109, 1, v84
	v_lshl_or_b32 v83, v84, 7, v89
	global_load_ushort v54, v109, s[14:15]
	global_load_dwordx4 v[28:31], v83, s[12:13]
	s_waitcnt vmcnt(6)
	v_cvt_f32_f16_e32 v55, v55
	v_cvt_f32_ubyte0_e32 v85, v32
	v_cvt_f32_ubyte1_e32 v86, v32
	v_cvt_f32_ubyte2_e32 v87, v32
	v_cvt_f32_ubyte3_e32 v88, v32
	v_fmac_f32_e32 v2, v85, v55
	v_fmac_f32_e32 v3, v86, v55
	v_fmac_f32_e32 v4, v87, v55
	v_fmac_f32_e32 v5, v88, v55
	v_cvt_f32_ubyte0_e32 v85, v33
	v_cvt_f32_ubyte1_e32 v86, v33
	v_cvt_f32_ubyte2_e32 v87, v33
	v_cvt_f32_ubyte3_e32 v88, v33
	v_fmac_f32_e32 v6, v85, v55
	v_fmac_f32_e32 v7, v86, v55
	v_fmac_f32_e32 v8, v87, v55
	v_fmac_f32_e32 v9, v88, v55
	v_cvt_f32_ubyte0_e32 v85, v34
	v_cvt_f32_ubyte1_e32 v86, v34
	v_cvt_f32_ubyte2_e32 v87, v34
	v_cvt_f32_ubyte3_e32 v88, v34
	v_fmac_f32_e32 v10, v85, v55
	v_fmac_f32_e32 v11, v86, v55
	v_fmac_f32_e32 v12, v87, v55
	v_fmac_f32_e32 v13, v88, v55
	v_cvt_f32_ubyte0_e32 v85, v35
	v_cvt_f32_ubyte1_e32 v86, v35
	v_cvt_f32_ubyte2_e32 v87, v35
	v_cvt_f32_ubyte3_e32 v88, v35
	v_fmac_f32_e32 v14, v85, v55
	v_fmac_f32_e32 v15, v86, v55
	v_fmac_f32_e32 v16, v87, v55
	v_fmac_f32_e32 v17, v88, v55
	v_add_f32_e32 v18, v18, v55
	v_lshrrev_b32_e32 v84, 16, v80
	v_lshlrev_b32_e32 v109, 1, v84
	v_lshl_or_b32 v83, v84, 7, v89
	global_load_ushort v55, v109, s[14:15]
	global_load_dwordx4 v[32:35], v83, s[12:13]
	s_cmp_le_u32 s40, 28
	s_cbranch_scc1 .Lg1_tail0
	s_waitcnt lgkmcnt(0)
	ds_bpermute_b32 v80, v90, v74 offset:28
	s_waitcnt vmcnt(6)
	v_cvt_f32_f16_e32 v52, v52
	v_cvt_f32_ubyte0_e32 v85, v20
	v_cvt_f32_ubyte1_e32 v86, v20
	v_cvt_f32_ubyte2_e32 v87, v20
	v_cvt_f32_ubyte3_e32 v88, v20
	v_fmac_f32_e32 v2, v85, v52
	v_fmac_f32_e32 v3, v86, v52
	v_fmac_f32_e32 v4, v87, v52
	v_fmac_f32_e32 v5, v88, v52
	v_cvt_f32_ubyte0_e32 v85, v21
	v_cvt_f32_ubyte1_e32 v86, v21
	v_cvt_f32_ubyte2_e32 v87, v21
	v_cvt_f32_ubyte3_e32 v88, v21
	v_fmac_f32_e32 v6, v85, v52
	v_fmac_f32_e32 v7, v86, v52
	v_fmac_f32_e32 v8, v87, v52
	v_fmac_f32_e32 v9, v88, v52
	v_cvt_f32_ubyte0_e32 v85, v22
	v_cvt_f32_ubyte1_e32 v86, v22
	v_cvt_f32_ubyte2_e32 v87, v22
	v_cvt_f32_ubyte3_e32 v88, v22
	v_fmac_f32_e32 v10, v85, v52
	v_fmac_f32_e32 v11, v86, v52
	v_fmac_f32_e32 v12, v87, v52
	v_fmac_f32_e32 v13, v88, v52
	v_cvt_f32_ubyte0_e32 v85, v23
	v_cvt_f32_ubyte1_e32 v86, v23
	v_cvt_f32_ubyte2_e32 v87, v23
	v_cvt_f32_ubyte3_e32 v88, v23
	v_fmac_f32_e32 v14, v85, v52
	v_fmac_f32_e32 v15, v86, v52
	v_fmac_f32_e32 v16, v87, v52
	v_fmac_f32_e32 v17, v88, v52
	v_add_f32_e32 v18, v18, v52
	v_and_b32_e32 v84, 0xffff, v79
	v_lshlrev_b32_e32 v109, 1, v84
	v_lshl_or_b32 v83, v84, 7, v89
	global_load_ushort v52, v109, s[14:15]
	global_load_dwordx4 v[20:23], v83, s[12:13]
	s_waitcnt vmcnt(6)
	v_cvt_f32_f16_e32 v53, v53
	v_cvt_f32_ubyte0_e32 v85, v24
	v_cvt_f32_ubyte1_e32 v86, v24
	v_cvt_f32_ubyte2_e32 v87, v24
	v_cvt_f32_ubyte3_e32 v88, v24
	v_fmac_f32_e32 v2, v85, v53
	v_fmac_f32_e32 v3, v86, v53
	v_fmac_f32_e32 v4, v87, v53
	v_fmac_f32_e32 v5, v88, v53
	v_cvt_f32_ubyte0_e32 v85, v25
	v_cvt_f32_ubyte1_e32 v86, v25
	v_cvt_f32_ubyte2_e32 v87, v25
	v_cvt_f32_ubyte3_e32 v88, v25
	v_fmac_f32_e32 v6, v85, v53
	v_fmac_f32_e32 v7, v86, v53
	v_fmac_f32_e32 v8, v87, v53
	v_fmac_f32_e32 v9, v88, v53
	v_cvt_f32_ubyte0_e32 v85, v26
	v_cvt_f32_ubyte1_e32 v86, v26
	v_cvt_f32_ubyte2_e32 v87, v26
	v_cvt_f32_ubyte3_e32 v88, v26
	v_fmac_f32_e32 v10, v85, v53
	v_fmac_f32_e32 v11, v86, v53
	v_fmac_f32_e32 v12, v87, v53
	v_fmac_f32_e32 v13, v88, v53
	v_cvt_f32_ubyte0_e32 v85, v27
	v_cvt_f32_ubyte1_e32 v86, v27
	v_cvt_f32_ubyte2_e32 v87, v27
	v_cvt_f32_ubyte3_e32 v88, v27
	v_fmac_f32_e32 v14, v85, v53
	v_fmac_f32_e32 v15, v86, v53
	v_fmac_f32_e32 v16, v87, v53
	v_fmac_f32_e32 v17, v88, v53
	v_add_f32_e32 v18, v18, v53
	v_lshrrev_b32_e32 v84, 16, v79
	v_lshlrev_b32_e32 v109, 1, v84
	v_lshl_or_b32 v83, v84, 7, v89
	global_load_ushort v53, v109, s[14:15]
	global_load_dwordx4 v[24:27], v83, s[12:13]
	s_cmp_le_u32 s40, 30
	s_cbranch_scc1 .Lg1_tail2
	s_waitcnt lgkmcnt(0)
	s_waitcnt vmcnt(6)
	v_cvt_f32_f16_e32 v54, v54
	v_cvt_f32_ubyte0_e32 v85, v28
	v_cvt_f32_ubyte1_e32 v86, v28
	v_cvt_f32_ubyte2_e32 v87, v28
	v_cvt_f32_ubyte3_e32 v88, v28
	v_fmac_f32_e32 v2, v85, v54
	v_fmac_f32_e32 v3, v86, v54
	v_fmac_f32_e32 v4, v87, v54
	v_fmac_f32_e32 v5, v88, v54
	v_cvt_f32_ubyte0_e32 v85, v29
	v_cvt_f32_ubyte1_e32 v86, v29
	v_cvt_f32_ubyte2_e32 v87, v29
	v_cvt_f32_ubyte3_e32 v88, v29
	v_fmac_f32_e32 v6, v85, v54
	v_fmac_f32_e32 v7, v86, v54
	v_fmac_f32_e32 v8, v87, v54
	v_fmac_f32_e32 v9, v88, v54
	v_cvt_f32_ubyte0_e32 v85, v30
	v_cvt_f32_ubyte1_e32 v86, v30
	v_cvt_f32_ubyte2_e32 v87, v30
	v_cvt_f32_ubyte3_e32 v88, v30
	v_fmac_f32_e32 v10, v85, v54
	v_fmac_f32_e32 v11, v86, v54
	v_fmac_f32_e32 v12, v87, v54
	v_fmac_f32_e32 v13, v88, v54
	v_cvt_f32_ubyte0_e32 v85, v31
	v_cvt_f32_ubyte1_e32 v86, v31
	v_cvt_f32_ubyte2_e32 v87, v31
	v_cvt_f32_ubyte3_e32 v88, v31
	v_fmac_f32_e32 v14, v85, v54
	v_fmac_f32_e32 v15, v86, v54
	v_fmac_f32_e32 v16, v87, v54
	v_fmac_f32_e32 v17, v88, v54
	v_add_f32_e32 v18, v18, v54
	v_and_b32_e32 v84, 0xffff, v80
	v_lshlrev_b32_e32 v109, 1, v84
	v_lshl_or_b32 v83, v84, 7, v89
	global_load_ushort v54, v109, s[14:15]
	global_load_dwordx4 v[28:31], v83, s[12:13]
	s_waitcnt vmcnt(6)
	v_cvt_f32_f16_e32 v55, v55
	v_cvt_f32_ubyte0_e32 v85, v32
	v_cvt_f32_ubyte1_e32 v86, v32
	v_cvt_f32_ubyte2_e32 v87, v32
	v_cvt_f32_ubyte3_e32 v88, v32
	v_fmac_f32_e32 v2, v85, v55
	v_fmac_f32_e32 v3, v86, v55
	v_fmac_f32_e32 v4, v87, v55
	v_fmac_f32_e32 v5, v88, v55
	v_cvt_f32_ubyte0_e32 v85, v33
	v_cvt_f32_ubyte1_e32 v86, v33
	v_cvt_f32_ubyte2_e32 v87, v33
	v_cvt_f32_ubyte3_e32 v88, v33
	v_fmac_f32_e32 v6, v85, v55
	v_fmac_f32_e32 v7, v86, v55
	v_fmac_f32_e32 v8, v87, v55
	v_fmac_f32_e32 v9, v88, v55
	v_cvt_f32_ubyte0_e32 v85, v34
	v_cvt_f32_ubyte1_e32 v86, v34
	v_cvt_f32_ubyte2_e32 v87, v34
	v_cvt_f32_ubyte3_e32 v88, v34
	v_fmac_f32_e32 v10, v85, v55
	v_fmac_f32_e32 v11, v86, v55
	v_fmac_f32_e32 v12, v87, v55
	v_fmac_f32_e32 v13, v88, v55
	v_cvt_f32_ubyte0_e32 v85, v35
	v_cvt_f32_ubyte1_e32 v86, v35
	v_cvt_f32_ubyte2_e32 v87, v35
	v_cvt_f32_ubyte3_e32 v88, v35
	v_fmac_f32_e32 v14, v85, v55
	v_fmac_f32_e32 v15, v86, v55
	v_fmac_f32_e32 v16, v87, v55
	v_fmac_f32_e32 v17, v88, v55
	v_add_f32_e32 v18, v18, v55
	v_lshrrev_b32_e32 v84, 16, v80
	v_lshlrev_b32_e32 v109, 1, v84
	v_lshl_or_b32 v83, v84, 7, v89
	global_load_ushort v55, v109, s[14:15]
	global_load_dwordx4 v[32:35], v83, s[12:13]

.Lg1_tail2:
	s_cmp_eq_u32 s39, 1
	s_cbranch_scc1 .Lg1_tailb2
	s_waitcnt vmcnt(6)
	v_cvt_f32_f16_e32 v54, v54
	v_cvt_f32_ubyte0_e32 v85, v28
	v_cvt_f32_ubyte1_e32 v86, v28
	v_cvt_f32_ubyte2_e32 v87, v28
	v_cvt_f32_ubyte3_e32 v88, v28
	v_fmac_f32_e32 v2, v85, v54
	v_fmac_f32_e32 v3, v86, v54
	v_fmac_f32_e32 v4, v87, v54
	v_fmac_f32_e32 v5, v88, v54
	v_cvt_f32_ubyte0_e32 v85, v29
	v_cvt_f32_ubyte1_e32 v86, v29
	v_cvt_f32_ubyte2_e32 v87, v29
	v_cvt_f32_ubyte3_e32 v88, v29
	v_fmac_f32_e32 v6, v85, v54
	v_fmac_f32_e32 v7, v86, v54
	v_fmac_f32_e32 v8, v87, v54
	v_fmac_f32_e32 v9, v88, v54
	v_cvt_f32_ubyte0_e32 v85, v30
	v_cvt_f32_ubyte1_e32 v86, v30
	v_cvt_f32_ubyte2_e32 v87, v30
	v_cvt_f32_ubyte3_e32 v88, v30
	v_fmac_f32_e32 v10, v85, v54
	v_fmac_f32_e32 v11, v86, v54
	v_fmac_f32_e32 v12, v87, v54
	v_fmac_f32_e32 v13, v88, v54
	v_cvt_f32_ubyte0_e32 v85, v31
	v_cvt_f32_ubyte1_e32 v86, v31
	v_cvt_f32_ubyte2_e32 v87, v31
	v_cvt_f32_ubyte3_e32 v88, v31
	v_fmac_f32_e32 v14, v85, v54
	v_fmac_f32_e32 v15, v86, v54
	v_fmac_f32_e32 v16, v87, v54
	v_fmac_f32_e32 v17, v88, v54
	v_add_f32_e32 v18, v18, v54
	s_waitcnt vmcnt(4)
	v_cvt_f32_f16_e32 v55, v55
	v_cvt_f32_ubyte0_e32 v85, v32
	v_cvt_f32_ubyte1_e32 v86, v32
	v_cvt_f32_ubyte2_e32 v87, v32
	v_cvt_f32_ubyte3_e32 v88, v32
	v_fmac_f32_e32 v2, v85, v55
	v_fmac_f32_e32 v3, v86, v55
	v_fmac_f32_e32 v4, v87, v55
	v_fmac_f32_e32 v5, v88, v55
	v_cvt_f32_ubyte0_e32 v85, v33
	v_cvt_f32_ubyte1_e32 v86, v33
	v_cvt_f32_ubyte2_e32 v87, v33
	v_cvt_f32_ubyte3_e32 v88, v33
	v_fmac_f32_e32 v6, v85, v55
	v_fmac_f32_e32 v7, v86, v55
	v_fmac_f32_e32 v8, v87, v55
	v_fmac_f32_e32 v9, v88, v55
	v_cvt_f32_ubyte0_e32 v85, v34
	v_cvt_f32_ubyte1_e32 v86, v34
	v_cvt_f32_ubyte2_e32 v87, v34
	v_cvt_f32_ubyte3_e32 v88, v34
	v_fmac_f32_e32 v10, v85, v55
	v_fmac_f32_e32 v11, v86, v55
	v_fmac_f32_e32 v12, v87, v55
	v_fmac_f32_e32 v13, v88, v55
	v_cvt_f32_ubyte0_e32 v85, v35
	v_cvt_f32_ubyte1_e32 v86, v35
	v_cvt_f32_ubyte2_e32 v87, v35
	v_cvt_f32_ubyte3_e32 v88, v35
	v_fmac_f32_e32 v14, v85, v55
	v_fmac_f32_e32 v15, v86, v55
	v_fmac_f32_e32 v16, v87, v55
	v_fmac_f32_e32 v17, v88, v55
	v_add_f32_e32 v18, v18, v55
	s_waitcnt vmcnt(2)
	v_cvt_f32_f16_e32 v52, v52
	v_cvt_f32_ubyte0_e32 v85, v20
	v_cvt_f32_ubyte1_e32 v86, v20
	v_cvt_f32_ubyte2_e32 v87, v20
	v_cvt_f32_ubyte3_e32 v88, v20
	v_fmac_f32_e32 v2, v85, v52
	v_fmac_f32_e32 v3, v86, v52
	v_fmac_f32_e32 v4, v87, v52
	v_fmac_f32_e32 v5, v88, v52
	v_cvt_f32_ubyte0_e32 v85, v21
	v_cvt_f32_ubyte1_e32 v86, v21
	v_cvt_f32_ubyte2_e32 v87, v21
	v_cvt_f32_ubyte3_e32 v88, v21
	v_fmac_f32_e32 v6, v85, v52
	v_fmac_f32_e32 v7, v86, v52
	v_fmac_f32_e32 v8, v87, v52
	v_fmac_f32_e32 v9, v88, v52
	v_cvt_f32_ubyte0_e32 v85, v22
	v_cvt_f32_ubyte1_e32 v86, v22
	v_cvt_f32_ubyte2_e32 v87, v22
	v_cvt_f32_ubyte3_e32 v88, v22
	v_fmac_f32_e32 v10, v85, v52
	v_fmac_f32_e32 v11, v86, v52
	v_fmac_f32_e32 v12, v87, v52
	v_fmac_f32_e32 v13, v88, v52
	v_cvt_f32_ubyte0_e32 v85, v23
	v_cvt_f32_ubyte1_e32 v86, v23
	v_cvt_f32_ubyte2_e32 v87, v23
	v_cvt_f32_ubyte3_e32 v88, v23
	v_fmac_f32_e32 v14, v85, v52
	v_fmac_f32_e32 v15, v86, v52
	v_fmac_f32_e32 v16, v87, v52
	v_fmac_f32_e32 v17, v88, v52
	v_add_f32_e32 v18, v18, v52
	s_waitcnt vmcnt(0)
	v_cvt_f32_f16_e32 v53, v53
	v_cvt_f32_ubyte0_e32 v85, v24
	v_cvt_f32_ubyte1_e32 v86, v24
	v_cvt_f32_ubyte2_e32 v87, v24
	v_cvt_f32_ubyte3_e32 v88, v24
	v_fmac_f32_e32 v2, v85, v53
	v_fmac_f32_e32 v3, v86, v53
	v_fmac_f32_e32 v4, v87, v53
	v_fmac_f32_e32 v5, v88, v53
	v_cvt_f32_ubyte0_e32 v85, v25
	v_cvt_f32_ubyte1_e32 v86, v25
	v_cvt_f32_ubyte2_e32 v87, v25
	v_cvt_f32_ubyte3_e32 v88, v25
	v_fmac_f32_e32 v6, v85, v53
	v_fmac_f32_e32 v7, v86, v53
	v_fmac_f32_e32 v8, v87, v53
	v_fmac_f32_e32 v9, v88, v53
	v_cvt_f32_ubyte0_e32 v85, v26
	v_cvt_f32_ubyte1_e32 v86, v26
	v_cvt_f32_ubyte2_e32 v87, v26
	v_cvt_f32_ubyte3_e32 v88, v26
	v_fmac_f32_e32 v10, v85, v53
	v_fmac_f32_e32 v11, v86, v53
	v_fmac_f32_e32 v12, v87, v53
	v_fmac_f32_e32 v13, v88, v53
	v_cvt_f32_ubyte0_e32 v85, v27
	v_cvt_f32_ubyte1_e32 v86, v27
	v_cvt_f32_ubyte2_e32 v87, v27
	v_cvt_f32_ubyte3_e32 v88, v27
	v_fmac_f32_e32 v14, v85, v53
	v_fmac_f32_e32 v15, v86, v53
	v_fmac_f32_e32 v16, v87, v53
	v_fmac_f32_e32 v17, v88, v53
	v_add_f32_e32 v18, v18, v53
	s_branch .Lg1_rare_check
.Lg1_tailb2:
	global_load_dwordx4 v[36:39], v103, s[8:9] offset:256
	global_load_dwordx4 v[40:43], v103, s[8:9] offset:272
	global_load_dwordx4 v[44:47], v103, s[8:9] offset:384
	global_load_dwordx4 v[48:51], v103, s[8:9] offset:400
	s_waitcnt vmcnt(10)
	v_cvt_f32_f16_e32 v54, v54
	v_cvt_f32_ubyte0_e32 v85, v28
	v_cvt_f32_ubyte1_e32 v86, v28
	v_cvt_f32_ubyte2_e32 v87, v28
	v_cvt_f32_ubyte3_e32 v88, v28
	v_fmac_f32_e32 v2, v85, v54
	v_fmac_f32_e32 v3, v86, v54
	v_fmac_f32_e32 v4, v87, v54
	v_fmac_f32_e32 v5, v88, v54
	v_cvt_f32_ubyte0_e32 v85, v29
	v_cvt_f32_ubyte1_e32 v86, v29
	v_cvt_f32_ubyte2_e32 v87, v29
	v_cvt_f32_ubyte3_e32 v88, v29
	v_fmac_f32_e32 v6, v85, v54
	v_fmac_f32_e32 v7, v86, v54
	v_fmac_f32_e32 v8, v87, v54
	v_fmac_f32_e32 v9, v88, v54
	v_cvt_f32_ubyte0_e32 v85, v30
	v_cvt_f32_ubyte1_e32 v86, v30
	v_cvt_f32_ubyte2_e32 v87, v30
	v_cvt_f32_ubyte3_e32 v88, v30
	v_fmac_f32_e32 v10, v85, v54
	v_fmac_f32_e32 v11, v86, v54
	v_fmac_f32_e32 v12, v87, v54
	v_fmac_f32_e32 v13, v88, v54
	v_cvt_f32_ubyte0_e32 v85, v31
	v_cvt_f32_ubyte1_e32 v86, v31
	v_cvt_f32_ubyte2_e32 v87, v31
	v_cvt_f32_ubyte3_e32 v88, v31
	v_fmac_f32_e32 v14, v85, v54
	v_fmac_f32_e32 v15, v86, v54
	v_fmac_f32_e32 v16, v87, v54
	v_fmac_f32_e32 v17, v88, v54
	v_add_f32_e32 v18, v18, v54
	global_load_dwordx4 v[28:31], v103, s[8:9] offset:128
	s_waitcnt vmcnt(9)
	v_cvt_f32_f16_e32 v55, v55
	v_cvt_f32_ubyte0_e32 v85, v32
	v_cvt_f32_ubyte1_e32 v86, v32
	v_cvt_f32_ubyte2_e32 v87, v32
	v_cvt_f32_ubyte3_e32 v88, v32
	v_fmac_f32_e32 v2, v85, v55
	v_fmac_f32_e32 v3, v86, v55
	v_fmac_f32_e32 v4, v87, v55
	v_fmac_f32_e32 v5, v88, v55
	v_cvt_f32_ubyte0_e32 v85, v33
	v_cvt_f32_ubyte1_e32 v86, v33
	v_cvt_f32_ubyte2_e32 v87, v33
	v_cvt_f32_ubyte3_e32 v88, v33
	v_fmac_f32_e32 v6, v85, v55
	v_fmac_f32_e32 v7, v86, v55
	v_fmac_f32_e32 v8, v87, v55
	v_fmac_f32_e32 v9, v88, v55
	v_cvt_f32_ubyte0_e32 v85, v34
	v_cvt_f32_ubyte1_e32 v86, v34
	v_cvt_f32_ubyte2_e32 v87, v34
	v_cvt_f32_ubyte3_e32 v88, v34
	v_fmac_f32_e32 v10, v85, v55
	v_fmac_f32_e32 v11, v86, v55
	v_fmac_f32_e32 v12, v87, v55
	v_fmac_f32_e32 v13, v88, v55
	v_cvt_f32_ubyte0_e32 v85, v35
	v_cvt_f32_ubyte1_e32 v86, v35
	v_cvt_f32_ubyte2_e32 v87, v35
	v_cvt_f32_ubyte3_e32 v88, v35
	v_fmac_f32_e32 v14, v85, v55
	v_fmac_f32_e32 v15, v86, v55
	v_fmac_f32_e32 v16, v87, v55
	v_fmac_f32_e32 v17, v88, v55
	v_add_f32_e32 v18, v18, v55
	global_load_dwordx4 v[32:35], v103, s[8:9] offset:144
	s_waitcnt vmcnt(8)
	v_cvt_f32_f16_e32 v52, v52
	v_cvt_f32_ubyte0_e32 v85, v20
	v_cvt_f32_ubyte1_e32 v86, v20
	v_cvt_f32_ubyte2_e32 v87, v20
	v_cvt_f32_ubyte3_e32 v88, v20
	v_fmac_f32_e32 v2, v85, v52
	v_fmac_f32_e32 v3, v86, v52
	v_fmac_f32_e32 v4, v87, v52
	v_fmac_f32_e32 v5, v88, v52
	v_cvt_f32_ubyte0_e32 v85, v21
	v_cvt_f32_ubyte1_e32 v86, v21
	v_cvt_f32_ubyte2_e32 v87, v21
	v_cvt_f32_ubyte3_e32 v88, v21
	v_fmac_f32_e32 v6, v85, v52
	v_fmac_f32_e32 v7, v86, v52
	v_fmac_f32_e32 v8, v87, v52
	v_fmac_f32_e32 v9, v88, v52
	v_cvt_f32_ubyte0_e32 v85, v22
	v_cvt_f32_ubyte1_e32 v86, v22
	v_cvt_f32_ubyte2_e32 v87, v22
	v_cvt_f32_ubyte3_e32 v88, v22
	v_fmac_f32_e32 v10, v85, v52
	v_fmac_f32_e32 v11, v86, v52
	v_fmac_f32_e32 v12, v87, v52
	v_fmac_f32_e32 v13, v88, v52
	v_cvt_f32_ubyte0_e32 v85, v23
	v_cvt_f32_ubyte1_e32 v86, v23
	v_cvt_f32_ubyte2_e32 v87, v23
	v_cvt_f32_ubyte3_e32 v88, v23
	v_fmac_f32_e32 v14, v85, v52
	v_fmac_f32_e32 v15, v86, v52
	v_fmac_f32_e32 v16, v87, v52
	v_fmac_f32_e32 v17, v88, v52
	v_add_f32_e32 v18, v18, v52
	global_load_dwordx4 v[20:23], v103, s[8:9] offset:0
	s_waitcnt vmcnt(7)
	v_cvt_f32_f16_e32 v53, v53
	v_cvt_f32_ubyte0_e32 v85, v24
	v_cvt_f32_ubyte1_e32 v86, v24
	v_cvt_f32_ubyte2_e32 v87, v24
	v_cvt_f32_ubyte3_e32 v88, v24
	v_fmac_f32_e32 v2, v85, v53
	v_fmac_f32_e32 v3, v86, v53
	v_fmac_f32_e32 v4, v87, v53
	v_fmac_f32_e32 v5, v88, v53
	v_cvt_f32_ubyte0_e32 v85, v25
	v_cvt_f32_ubyte1_e32 v86, v25
	v_cvt_f32_ubyte2_e32 v87, v25
	v_cvt_f32_ubyte3_e32 v88, v25
	v_fmac_f32_e32 v6, v85, v53
	v_fmac_f32_e32 v7, v86, v53
	v_fmac_f32_e32 v8, v87, v53
	v_fmac_f32_e32 v9, v88, v53
	v_cvt_f32_ubyte0_e32 v85, v26
	v_cvt_f32_ubyte1_e32 v86, v26
	v_cvt_f32_ubyte2_e32 v87, v26
	v_cvt_f32_ubyte3_e32 v88, v26
	v_fmac_f32_e32 v10, v85, v53
	v_fmac_f32_e32 v11, v86, v53
	v_fmac_f32_e32 v12, v87, v53
	v_fmac_f32_e32 v13, v88, v53
	v_cvt_f32_ubyte0_e32 v85, v27
	v_cvt_f32_ubyte1_e32 v86, v27
	v_cvt_f32_ubyte2_e32 v87, v27
	v_cvt_f32_ubyte3_e32 v88, v27
	v_fmac_f32_e32 v14, v85, v53
	v_fmac_f32_e32 v15, v86, v53
	v_fmac_f32_e32 v16, v87, v53
	v_fmac_f32_e32 v17, v88, v53
	v_add_f32_e32 v18, v18, v53
	global_load_dwordx4 v[24:27], v103, s[8:9] offset:16
	s_branch .Lg1_rare_check

.Lg2_active:
	s_mov_b32 s46, 0x01010101
	s_mov_b32 s47, 0x01010101
	s_mov_b32 s60, 0x00ff00ff
	s_mov_b32 s61, 0x0c030c01
	v_lshrrev_b32_e32 v107, 3, v1
	v_and_b32_e32 v108, 7, v1
	v_and_b32_e32 v105, 15, v1
	v_lshrrev_b32_e32 v106, 4, v1
	s_bfe_u32 s36, s3, 0x10002
	s_lshl_b32 s58, s36, 3
	s_xor_b32 s59, s58, 8
	v_or_b32_e32 v102, s58, v107
	v_or_b32_e32 v103, s59, v107
	v_lshlrev_b32_e32 v89, 4, v108
	v_and_b32_e32 v90, 56, v1
	v_lshlrev_b32_e32 v90, 2, v90
	s_waitcnt lgkmcnt(0)
	s_lshl_b32 s58, s6, 8
	s_add_u32 s32, s16, s58
	s_addc_u32 s33, s17, 0
	s_lshl_b32 s58, s6, 10
	s_add_u32 s34, s18, s58
	s_addc_u32 s35, s19, 0
	v_lshlrev_b32_e32 v109, 4, v105
	global_load_dword v104, v109, s[32:33] offset:8
	v_lshlrev_b32_e32 v110, 4, v102
	global_load_dwordx2 v[68:69], v110, s[32:33]
	v_lshlrev_b32_e32 v111, 4, v103
	global_load_dwordx2 v[70:71], v111, s[32:33]
	v_lshlrev_b32_e32 v101, 2, v108
	v_lshl_or_b32 v110, v102, 6, v101
	global_load_dword v60, v110, s[34:35]
	global_load_dword v61, v110, s[34:35] offset:32
	v_lshl_or_b32 v111, v103, 6, v101
	global_load_dword v62, v111, s[34:35]
	global_load_dword v63, v111, s[34:35] offset:32
	global_load_dwordx4 v[2:5], v95, s[22:23]
	global_load_dwordx4 v[6:9], v98, s[22:23]
	global_load_dwordx4 v[10:13], v99, s[22:23]
	global_load_dwordx4 v[14:17], v100, s[22:23]
	v_and_b32_e32 v101, 0x7f, v0
	v_lshlrev_b32_e32 v101, 2, v101
	global_load_dword v19, v101, s[24:25]
	s_mul_i32 s48, s3, 0x1100
	s_add_u32 s48, s48, 66048
	v_mul_u32_u24_e32 v91, 0x110, v102
	v_lshl_add_u32 v91, v108, 5, v91
	v_add_u32_e32 v91, s48, v91
	v_mul_u32_u24_e32 v92, 0x110, v103
	v_lshl_add_u32 v92, v108, 5, v92
	v_add_u32_e32 v92, s48, v92
	s_waitcnt vmcnt(5)
	v_readlane_b32 s49, v69, 0
	v_readlane_b32 s50, v69, 8
	v_readlane_b32 s51, v69, 16
	v_readlane_b32 s52, v69, 24
	v_readlane_b32 s53, v69, 32
	v_readlane_b32 s54, v69, 40
	v_readlane_b32 s55, v69, 48
	v_readlane_b32 s56, v69, 56
	s_max_i32 s37, s49, s50
	s_max_i32 s37, s37, s51
	s_max_i32 s37, s37, s52
	s_max_i32 s37, s37, s53
	s_max_i32 s37, s37, s54
	s_max_i32 s37, s37, s55
	s_max_i32 s37, s37, s56
	v_readlane_b32 s49, v71, 0
	v_readlane_b32 s50, v71, 8
	v_readlane_b32 s51, v71, 16
	v_readlane_b32 s52, v71, 24
	v_readlane_b32 s53, v71, 32
	v_readlane_b32 s54, v71, 40
	v_readlane_b32 s55, v71, 48
	v_readlane_b32 s56, v71, 56
	s_max_i32 s38, s49, s50
	s_max_i32 s38, s38, s51
	s_max_i32 s38, s38, s52
	s_max_i32 s38, s38, s53
	s_max_i32 s38, s38, s54
	s_max_i32 s38, s38, s55
	s_max_i32 s38, s38, s56
	v_lshlrev_b32_e32 v103, 8, v104
	v_lshl_or_b32 v103, v106, 4, v103
	s_waitcnt vmcnt(0)
	ds_write_b128 v96, v[2:5]
	ds_write_b128 v96, v[6:9] offset:16384
	ds_write_b128 v96, v[10:13] offset:32768
	ds_write_b128 v96, v[14:17] offset:49152
	v_add_u32_e32 v101, 0x10000, v101
	ds_write_b32 v101, v19
	s_mov_b32 s39, 0

.Lg2_sel_done:
	s_min_i32 s40, s41, 32
	s_add_i32 s40, s40, 1
	s_and_b32 s40, s40, 62
	s_max_i32 s40, s40, 4
	v_mov_b32_e32 v2, 0
	v_mov_b32_e32 v3, 0
	v_mov_b32_e32 v4, 0
	v_mov_b32_e32 v5, 0
	v_mov_b32_e32 v6, 0
	v_mov_b32_e32 v7, 0
	v_mov_b32_e32 v8, 0
	v_mov_b32_e32 v9, 0
	v_mov_b32_e32 v10, 0
	v_mov_b32_e32 v11, 0
	v_mov_b32_e32 v12, 0
	v_mov_b32_e32 v13, 0
	v_mov_b32_e32 v14, 0
	v_mov_b32_e32 v15, 0
	v_mov_b32_e32 v16, 0
	v_mov_b32_e32 v17, 0
	s_waitcnt lgkmcnt(0)
	ds_bpermute_b32 v94, v90, v73 offset:0
	ds_bpermute_b32 v95, v90, v73 offset:4
	ds_bpermute_b32 v79, v90, v73 offset:8
	s_waitcnt lgkmcnt(1)
	v_and_b32_e32 v84, 0xffff, v94
	v_lshlrev_b32_e32 v109, 1, v84
	v_lshl_or_b32 v83, v84, 7, v89
	global_load_ushort v52, v109, s[14:15]
	global_load_dwordx4 v[20:23], v83, s[12:13]
	v_lshrrev_b32_e32 v84, 16, v94
	v_lshlrev_b32_e32 v109, 1, v84
	v_lshl_or_b32 v83, v84, 7, v89
	global_load_ushort v53, v109, s[14:15]
	global_load_dwordx4 v[24:27], v83, s[12:13]
	v_and_b32_e32 v84, 0xffff, v95
	v_lshlrev_b32_e32 v109, 1, v84
	v_lshl_or_b32 v83, v84, 7, v89
	global_load_ushort v54, v109, s[14:15]
	global_load_dwordx4 v[28:31], v83, s[12:13]
	v_lshrrev_b32_e32 v84, 16, v95
	v_lshlrev_b32_e32 v109, 1, v84
	v_lshl_or_b32 v83, v84, 7, v89
	global_load_ushort v55, v109, s[14:15]
	global_load_dwordx4 v[32:35], v83, s[12:13]
	s_cmp_eq_u32 s39, 0
	s_cbranch_scc0 .Lg2_nobar
	s_waitcnt lgkmcnt(0)
	s_barrier
.Lg2_nobar:
	s_cmp_le_u32 s40, 4
	s_cbranch_scc1 .Lg2_tail0
	s_waitcnt lgkmcnt(0)
	ds_bpermute_b32 v80, v90, v73 offset:12
	s_waitcnt vmcnt(6)
	v_cvt_f32_f16_e32 v52, v52
	v_cvt_f32_ubyte0_e32 v85, v20
	v_cvt_f32_ubyte1_e32 v86, v20
	v_cvt_f32_ubyte2_e32 v87, v20
	v_cvt_f32_ubyte3_e32 v88, v20
	v_fmac_f32_e32 v2, v85, v52
	v_fmac_f32_e32 v3, v86, v52
	v_fmac_f32_e32 v4, v87, v52
	v_fmac_f32_e32 v5, v88, v52
	v_cvt_f32_ubyte0_e32 v85, v21
	v_cvt_f32_ubyte1_e32 v86, v21
	v_cvt_f32_ubyte2_e32 v87, v21
	v_cvt_f32_ubyte3_e32 v88, v21
	v_fmac_f32_e32 v6, v85, v52
	v_fmac_f32_e32 v7, v86, v52
	v_fmac_f32_e32 v8, v87, v52
	v_fmac_f32_e32 v9, v88, v52
	v_cvt_f32_ubyte0_e32 v85, v22
	v_cvt_f32_ubyte1_e32 v86, v22
	v_cvt_f32_ubyte2_e32 v87, v22
	v_cvt_f32_ubyte3_e32 v88, v22
	v_fmac_f32_e32 v10, v85, v52
	v_fmac_f32_e32 v11, v86, v52
	v_fmac_f32_e32 v12, v87, v52
	v_fmac_f32_e32 v13, v88, v52
	v_cvt_f32_ubyte0_e32 v85, v23
	v_cvt_f32_ubyte1_e32 v86, v23
	v_cvt_f32_ubyte2_e32 v87, v23
	v_cvt_f32_ubyte3_e32 v88, v23
	v_fmac_f32_e32 v14, v85, v52
	v_fmac_f32_e32 v15, v86, v52
	v_fmac_f32_e32 v16, v87, v52
	v_fmac_f32_e32 v17, v88, v52
	v_and_b32_e32 v84, 0xffff, v79
	v_lshlrev_b32_e32 v109, 1, v84
	v_lshl_or_b32 v83, v84, 7, v89
	global_load_ushort v52, v109, s[14:15]
	global_load_dwordx4 v[20:23], v83, s[12:13]
	s_waitcnt vmcnt(6)
	v_cvt_f32_f16_e32 v53, v53
	v_cvt_f32_ubyte0_e32 v85, v24
	v_cvt_f32_ubyte1_e32 v86, v24
	v_cvt_f32_ubyte2_e32 v87, v24
	v_cvt_f32_ubyte3_e32 v88, v24
	v_fmac_f32_e32 v2, v85, v53
	v_fmac_f32_e32 v3, v86, v53
	v_fmac_f32_e32 v4, v87, v53
	v_fmac_f32_e32 v5, v88, v53
	v_cvt_f32_ubyte0_e32 v85, v25
	v_cvt_f32_ubyte1_e32 v86, v25
	v_cvt_f32_ubyte2_e32 v87, v25
	v_cvt_f32_ubyte3_e32 v88, v25
	v_fmac_f32_e32 v6, v85, v53
	v_fmac_f32_e32 v7, v86, v53
	v_fmac_f32_e32 v8, v87, v53
	v_fmac_f32_e32 v9, v88, v53
	v_cvt_f32_ubyte0_e32 v85, v26
	v_cvt_f32_ubyte1_e32 v86, v26
	v_cvt_f32_ubyte2_e32 v87, v26
	v_cvt_f32_ubyte3_e32 v88, v26
	v_fmac_f32_e32 v10, v85, v53
	v_fmac_f32_e32 v11, v86, v53
	v_fmac_f32_e32 v12, v87, v53
	v_fmac_f32_e32 v13, v88, v53
	v_cvt_f32_ubyte0_e32 v85, v27
	v_cvt_f32_ubyte1_e32 v86, v27
	v_cvt_f32_ubyte2_e32 v87, v27
	v_cvt_f32_ubyte3_e32 v88, v27
	v_fmac_f32_e32 v14, v85, v53
	v_fmac_f32_e32 v15, v86, v53
	v_fmac_f32_e32 v16, v87, v53
	v_fmac_f32_e32 v17, v88, v53
	v_lshrrev_b32_e32 v84, 16, v79
	v_lshlrev_b32_e32 v109, 1, v84
	v_lshl_or_b32 v83, v84, 7, v89
	global_load_ushort v53, v109, s[14:15]
	global_load_dwordx4 v[24:27], v83, s[12:13]
	s_cmp_le_u32 s40, 6
	s_cbranch_scc1 .Lg2_tail2
	s_waitcnt lgkmcnt(0)
	ds_bpermute_b32 v79, v90, v73 offset:16
	s_waitcnt vmcnt(6)
	v_cvt_f32_f16_e32 v54, v54
	v_cvt_f32_ubyte0_e32 v85, v28
	v_cvt_f32_ubyte1_e32 v86, v28
	v_cvt_f32_ubyte2_e32 v87, v28
	v_cvt_f32_ubyte3_e32 v88, v28
	v_fmac_f32_e32 v2, v85, v54
	v_fmac_f32_e32 v3, v86, v54
	v_fmac_f32_e32 v4, v87, v54
	v_fmac_f32_e32 v5, v88, v54
	v_cvt_f32_ubyte0_e32 v85, v29
	v_cvt_f32_ubyte1_e32 v86, v29
	v_cvt_f32_ubyte2_e32 v87, v29
	v_cvt_f32_ubyte3_e32 v88, v29
	v_fmac_f32_e32 v6, v85, v54
	v_fmac_f32_e32 v7, v86, v54
	v_fmac_f32_e32 v8, v87, v54
	v_fmac_f32_e32 v9, v88, v54
	v_cvt_f32_ubyte0_e32 v85, v30
	v_cvt_f32_ubyte1_e32 v86, v30
	v_cvt_f32_ubyte2_e32 v87, v30
	v_cvt_f32_ubyte3_e32 v88, v30
	v_fmac_f32_e32 v10, v85, v54
	v_fmac_f32_e32 v11, v86, v54
	v_fmac_f32_e32 v12, v87, v54
	v_fmac_f32_e32 v13, v88, v54
	v_cvt_f32_ubyte0_e32 v85, v31
	v_cvt_f32_ubyte1_e32 v86, v31
	v_cvt_f32_ubyte2_e32 v87, v31
	v_cvt_f32_ubyte3_e32 v88, v31
	v_fmac_f32_e32 v14, v85, v54
	v_fmac_f32_e32 v15, v86, v54
	v_fmac_f32_e32 v16, v87, v54
	v_fmac_f32_e32 v17, v88, v54
	v_and_b32_e32 v84, 0xffff, v80
	v_lshlrev_b32_e32 v109, 1, v84
	v_lshl_or_b32 v83, v84, 7, v89
	global_load_ushort v54, v109, s[14:15]
	global_load_dwordx4 v[28:31], v83, s[12:13]
	s_waitcnt vmcnt(6)
	v_cvt_f32_f16_e32 v55, v55
	v_cvt_f32_ubyte0_e32 v85, v32
	v_cvt_f32_ubyte1_e32 v86, v32
	v_cvt_f32_ubyte2_e32 v87, v32
	v_cvt_f32_ubyte3_e32 v88, v32
	v_fmac_f32_e32 v2, v85, v55
	v_fmac_f32_e32 v3, v86, v55
	v_fmac_f32_e32 v4, v87, v55
	v_fmac_f32_e32 v5, v88, v55
	v_cvt_f32_ubyte0_e32 v85, v33
	v_cvt_f32_ubyte1_e32 v86, v33
	v_cvt_f32_ubyte2_e32 v87, v33
	v_cvt_f32_ubyte3_e32 v88, v33
	v_fmac_f32_e32 v6, v85, v55
	v_fmac_f32_e32 v7, v86, v55
	v_fmac_f32_e32 v8, v87, v55
	v_fmac_f32_e32 v9, v88, v55
	v_cvt_f32_ubyte0_e32 v85, v34
	v_cvt_f32_ubyte1_e32 v86, v34
	v_cvt_f32_ubyte2_e32 v87, v34
	v_cvt_f32_ubyte3_e32 v88, v34
	v_fmac_f32_e32 v10, v85, v55
	v_fmac_f32_e32 v11, v86, v55
	v_fmac_f32_e32 v12, v87, v55
	v_fmac_f32_e32 v13, v88, v55
	v_cvt_f32_ubyte0_e32 v85, v35
	v_cvt_f32_ubyte1_e32 v86, v35
	v_cvt_f32_ubyte2_e32 v87, v35
	v_cvt_f32_ubyte3_e32 v88, v35
	v_fmac_f32_e32 v14, v85, v55
	v_fmac_f32_e32 v15, v86, v55
	v_fmac_f32_e32 v16, v87, v55
	v_fmac_f32_e32 v17, v88, v55
	v_lshrrev_b32_e32 v84, 16, v80
	v_lshlrev_b32_e32 v109, 1, v84
	v_lshl_or_b32 v83, v84, 7, v89
	global_load_ushort v55, v109, s[14:15]
	global_load_dwordx4 v[32:35], v83, s[12:13]
	s_cmp_le_u32 s40, 8
	s_cbranch_scc1 .Lg2_tail0
	s_waitcnt lgkmcnt(0)
	ds_bpermute_b32 v80, v90, v73 offset:20
	s_waitcnt vmcnt(6)
	v_cvt_f32_f16_e32 v52, v52
	v_cvt_f32_ubyte0_e32 v85, v20
	v_cvt_f32_ubyte1_e32 v86, v20
	v_cvt_f32_ubyte2_e32 v87, v20
	v_cvt_f32_ubyte3_e32 v88, v20
	v_fmac_f32_e32 v2, v85, v52
	v_fmac_f32_e32 v3, v86, v52
	v_fmac_f32_e32 v4, v87, v52
	v_fmac_f32_e32 v5, v88, v52
	v_cvt_f32_ubyte0_e32 v85, v21
	v_cvt_f32_ubyte1_e32 v86, v21
	v_cvt_f32_ubyte2_e32 v87, v21
	v_cvt_f32_ubyte3_e32 v88, v21
	v_fmac_f32_e32 v6, v85, v52
	v_fmac_f32_e32 v7, v86, v52
	v_fmac_f32_e32 v8, v87, v52
	v_fmac_f32_e32 v9, v88, v52
	v_cvt_f32_ubyte0_e32 v85, v22
	v_cvt_f32_ubyte1_e32 v86, v22
	v_cvt_f32_ubyte2_e32 v87, v22
	v_cvt_f32_ubyte3_e32 v88, v22
	v_fmac_f32_e32 v10, v85, v52
	v_fmac_f32_e32 v11, v86, v52
	v_fmac_f32_e32 v12, v87, v52
	v_fmac_f32_e32 v13, v88, v52
	v_cvt_f32_ubyte0_e32 v85, v23
	v_cvt_f32_ubyte1_e32 v86, v23
	v_cvt_f32_ubyte2_e32 v87, v23
	v_cvt_f32_ubyte3_e32 v88, v23
	v_fmac_f32_e32 v14, v85, v52
	v_fmac_f32_e32 v15, v86, v52
	v_fmac_f32_e32 v16, v87, v52
	v_fmac_f32_e32 v17, v88, v52
	v_and_b32_e32 v84, 0xffff, v79
	v_lshlrev_b32_e32 v109, 1, v84
	v_lshl_or_b32 v83, v84, 7, v89
	global_load_ushort v52, v109, s[14:15]
	global_load_dwordx4 v[20:23], v83, s[12:13]
	s_waitcnt vmcnt(6)
	v_cvt_f32_f16_e32 v53, v53
	v_cvt_f32_ubyte0_e32 v85, v24
	v_cvt_f32_ubyte1_e32 v86, v24
	v_cvt_f32_ubyte2_e32 v87, v24
	v_cvt_f32_ubyte3_e32 v88, v24
	v_fmac_f32_e32 v2, v85, v53
	v_fmac_f32_e32 v3, v86, v53
	v_fmac_f32_e32 v4, v87, v53
	v_fmac_f32_e32 v5, v88, v53
	v_cvt_f32_ubyte0_e32 v85, v25
	v_cvt_f32_ubyte1_e32 v86, v25
	v_cvt_f32_ubyte2_e32 v87, v25
	v_cvt_f32_ubyte3_e32 v88, v25
	v_fmac_f32_e32 v6, v85, v53
	v_fmac_f32_e32 v7, v86, v53
	v_fmac_f32_e32 v8, v87, v53
	v_fmac_f32_e32 v9, v88, v53
	v_cvt_f32_ubyte0_e32 v85, v26
	v_cvt_f32_ubyte1_e32 v86, v26
	v_cvt_f32_ubyte2_e32 v87, v26
	v_cvt_f32_ubyte3_e32 v88, v26
	v_fmac_f32_e32 v10, v85, v53
	v_fmac_f32_e32 v11, v86, v53
	v_fmac_f32_e32 v12, v87, v53
	v_fmac_f32_e32 v13, v88, v53
	v_cvt_f32_ubyte0_e32 v85, v27
	v_cvt_f32_ubyte1_e32 v86, v27
	v_cvt_f32_ubyte2_e32 v87, v27
	v_cvt_f32_ubyte3_e32 v88, v27
	v_fmac_f32_e32 v14, v85, v53
	v_fmac_f32_e32 v15, v86, v53
	v_fmac_f32_e32 v16, v87, v53
	v_fmac_f32_e32 v17, v88, v53
	v_lshrrev_b32_e32 v84, 16, v79
	v_lshlrev_b32_e32 v109, 1, v84
	v_lshl_or_b32 v83, v84, 7, v89
	global_load_ushort v53, v109, s[14:15]
	global_load_dwordx4 v[24:27], v83, s[12:13]
	s_cmp_le_u32 s40, 10
	s_cbranch_scc1 .Lg2_tail2
	s_waitcnt lgkmcnt(0)
	ds_bpermute_b32 v79, v90, v73 offset:24
	s_waitcnt vmcnt(6)
	v_cvt_f32_f16_e32 v54, v54
	v_cvt_f32_ubyte0_e32 v85, v28
	v_cvt_f32_ubyte1_e32 v86, v28
	v_cvt_f32_ubyte2_e32 v87, v28
	v_cvt_f32_ubyte3_e32 v88, v28
	v_fmac_f32_e32 v2, v85, v54
	v_fmac_f32_e32 v3, v86, v54
	v_fmac_f32_e32 v4, v87, v54
	v_fmac_f32_e32 v5, v88, v54
	v_cvt_f32_ubyte0_e32 v85, v29
	v_cvt_f32_ubyte1_e32 v86, v29
	v_cvt_f32_ubyte2_e32 v87, v29
	v_cvt_f32_ubyte3_e32 v88, v29
	v_fmac_f32_e32 v6, v85, v54
	v_fmac_f32_e32 v7, v86, v54
	v_fmac_f32_e32 v8, v87, v54
	v_fmac_f32_e32 v9, v88, v54
	v_cvt_f32_ubyte0_e32 v85, v30
	v_cvt_f32_ubyte1_e32 v86, v30
	v_cvt_f32_ubyte2_e32 v87, v30
	v_cvt_f32_ubyte3_e32 v88, v30
	v_fmac_f32_e32 v10, v85, v54
	v_fmac_f32_e32 v11, v86, v54
	v_fmac_f32_e32 v12, v87, v54
	v_fmac_f32_e32 v13, v88, v54
	v_cvt_f32_ubyte0_e32 v85, v31
	v_cvt_f32_ubyte1_e32 v86, v31
	v_cvt_f32_ubyte2_e32 v87, v31
	v_cvt_f32_ubyte3_e32 v88, v31
	v_fmac_f32_e32 v14, v85, v54
	v_fmac_f32_e32 v15, v86, v54
	v_fmac_f32_e32 v16, v87, v54
	v_fmac_f32_e32 v17, v88, v54
	v_and_b32_e32 v84, 0xffff, v80
	v_lshlrev_b32_e32 v109, 1, v84
	v_lshl_or_b32 v83, v84, 7, v89
	global_load_ushort v54, v109, s[14:15]
	global_load_dwordx4 v[28:31], v83, s[12:13]
	s_waitcnt vmcnt(6)
	v_cvt_f32_f16_e32 v55, v55
	v_cvt_f32_ubyte0_e32 v85, v32
	v_cvt_f32_ubyte1_e32 v86, v32
	v_cvt_f32_ubyte2_e32 v87, v32
	v_cvt_f32_ubyte3_e32 v88, v32
	v_fmac_f32_e32 v2, v85, v55
	v_fmac_f32_e32 v3, v86, v55
	v_fmac_f32_e32 v4, v87, v55
	v_fmac_f32_e32 v5, v88, v55
	v_cvt_f32_ubyte0_e32 v85, v33
	v_cvt_f32_ubyte1_e32 v86, v33
	v_cvt_f32_ubyte2_e32 v87, v33
	v_cvt_f32_ubyte3_e32 v88, v33
	v_fmac_f32_e32 v6, v85, v55
	v_fmac_f32_e32 v7, v86, v55
	v_fmac_f32_e32 v8, v87, v55
	v_fmac_f32_e32 v9, v88, v55
	v_cvt_f32_ubyte0_e32 v85, v34
	v_cvt_f32_ubyte1_e32 v86, v34
	v_cvt_f32_ubyte2_e32 v87, v34
	v_cvt_f32_ubyte3_e32 v88, v34
	v_fmac_f32_e32 v10, v85, v55
	v_fmac_f32_e32 v11, v86, v55
	v_fmac_f32_e32 v12, v87, v55
	v_fmac_f32_e32 v13, v88, v55
	v_cvt_f32_ubyte0_e32 v85, v35
	v_cvt_f32_ubyte1_e32 v86, v35
	v_cvt_f32_ubyte2_e32 v87, v35
	v_cvt_f32_ubyte3_e32 v88, v35
	v_fmac_f32_e32 v14, v85, v55
	v_fmac_f32_e32 v15, v86, v55
	v_fmac_f32_e32 v16, v87, v55
	v_fmac_f32_e32 v17, v88, v55
	v_lshrrev_b32_e32 v84, 16, v80
	v_lshlrev_b32_e32 v109, 1, v84
	v_lshl_or_b32 v83, v84, 7, v89
	global_load_ushort v55, v109, s[14:15]
	global_load_dwordx4 v[32:35], v83, s[12:13]
	s_cmp_le_u32 s40, 12
	s_cbranch_scc1 .Lg2_tail0
	s_waitcnt lgkmcnt(0)
	ds_bpermute_b32 v80, v90, v73 offset:28
	s_waitcnt vmcnt(6)
	v_cvt_f32_f16_e32 v52, v52
	v_cvt_f32_ubyte0_e32 v85, v20
	v_cvt_f32_ubyte1_e32 v86, v20
	v_cvt_f32_ubyte2_e32 v87, v20
	v_cvt_f32_ubyte3_e32 v88, v20
	v_fmac_f32_e32 v2, v85, v52
	v_fmac_f32_e32 v3, v86, v52
	v_fmac_f32_e32 v4, v87, v52
	v_fmac_f32_e32 v5, v88, v52
	v_cvt_f32_ubyte0_e32 v85, v21
	v_cvt_f32_ubyte1_e32 v86, v21
	v_cvt_f32_ubyte2_e32 v87, v21
	v_cvt_f32_ubyte3_e32 v88, v21
	v_fmac_f32_e32 v6, v85, v52
	v_fmac_f32_e32 v7, v86, v52
	v_fmac_f32_e32 v8, v87, v52
	v_fmac_f32_e32 v9, v88, v52
	v_cvt_f32_ubyte0_e32 v85, v22
	v_cvt_f32_ubyte1_e32 v86, v22
	v_cvt_f32_ubyte2_e32 v87, v22
	v_cvt_f32_ubyte3_e32 v88, v22
	v_fmac_f32_e32 v10, v85, v52
	v_fmac_f32_e32 v11, v86, v52
	v_fmac_f32_e32 v12, v87, v52
	v_fmac_f32_e32 v13, v88, v52
	v_cvt_f32_ubyte0_e32 v85, v23
	v_cvt_f32_ubyte1_e32 v86, v23
	v_cvt_f32_ubyte2_e32 v87, v23
	v_cvt_f32_ubyte3_e32 v88, v23
	v_fmac_f32_e32 v14, v85, v52
	v_fmac_f32_e32 v15, v86, v52
	v_fmac_f32_e32 v16, v87, v52
	v_fmac_f32_e32 v17, v88, v52
	v_and_b32_e32 v84, 0xffff, v79
	v_lshlrev_b32_e32 v109, 1, v84
	v_lshl_or_b32 v83, v84, 7, v89
	global_load_ushort v52, v109, s[14:15]
	global_load_dwordx4 v[20:23], v83, s[12:13]
	s_waitcnt vmcnt(6)
	v_cvt_f32_f16_e32 v53, v53
	v_cvt_f32_ubyte0_e32 v85, v24
	v_cvt_f32_ubyte1_e32 v86, v24
	v_cvt_f32_ubyte2_e32 v87, v24
	v_cvt_f32_ubyte3_e32 v88, v24
	v_fmac_f32_e32 v2, v85, v53
	v_fmac_f32_e32 v3, v86, v53
	v_fmac_f32_e32 v4, v87, v53
	v_fmac_f32_e32 v5, v88, v53
	v_cvt_f32_ubyte0_e32 v85, v25
	v_cvt_f32_ubyte1_e32 v86, v25
	v_cvt_f32_ubyte2_e32 v87, v25
	v_cvt_f32_ubyte3_e32 v88, v25
	v_fmac_f32_e32 v6, v85, v53
	v_fmac_f32_e32 v7, v86, v53
	v_fmac_f32_e32 v8, v87, v53
	v_fmac_f32_e32 v9, v88, v53
	v_cvt_f32_ubyte0_e32 v85, v26
	v_cvt_f32_ubyte1_e32 v86, v26
	v_cvt_f32_ubyte2_e32 v87, v26
	v_cvt_f32_ubyte3_e32 v88, v26
	v_fmac_f32_e32 v10, v85, v53
	v_fmac_f32_e32 v11, v86, v53
	v_fmac_f32_e32 v12, v87, v53
	v_fmac_f32_e32 v13, v88, v53
	v_cvt_f32_ubyte0_e32 v85, v27
	v_cvt_f32_ubyte1_e32 v86, v27
	v_cvt_f32_ubyte2_e32 v87, v27
	v_cvt_f32_ubyte3_e32 v88, v27
	v_fmac_f32_e32 v14, v85, v53
	v_fmac_f32_e32 v15, v86, v53
	v_fmac_f32_e32 v16, v87, v53
	v_fmac_f32_e32 v17, v88, v53
	v_lshrrev_b32_e32 v84, 16, v79
	v_lshlrev_b32_e32 v109, 1, v84
	v_lshl_or_b32 v83, v84, 7, v89
	global_load_ushort v53, v109, s[14:15]
	global_load_dwordx4 v[24:27], v83, s[12:13]
	s_cmp_le_u32 s40, 14
	s_cbranch_scc1 .Lg2_tail2
	s_waitcnt lgkmcnt(0)
	ds_bpermute_b32 v79, v90, v74 offset:0
	s_waitcnt vmcnt(6)
	v_cvt_f32_f16_e32 v54, v54
	v_cvt_f32_ubyte0_e32 v85, v28
	v_cvt_f32_ubyte1_e32 v86, v28
	v_cvt_f32_ubyte2_e32 v87, v28
	v_cvt_f32_ubyte3_e32 v88, v28
	v_fmac_f32_e32 v2, v85, v54
	v_fmac_f32_e32 v3, v86, v54
	v_fmac_f32_e32 v4, v87, v54
	v_fmac_f32_e32 v5, v88, v54
	v_cvt_f32_ubyte0_e32 v85, v29
	v_cvt_f32_ubyte1_e32 v86, v29
	v_cvt_f32_ubyte2_e32 v87, v29
	v_cvt_f32_ubyte3_e32 v88, v29
	v_fmac_f32_e32 v6, v85, v54
	v_fmac_f32_e32 v7, v86, v54
	v_fmac_f32_e32 v8, v87, v54
	v_fmac_f32_e32 v9, v88, v54
	v_cvt_f32_ubyte0_e32 v85, v30
	v_cvt_f32_ubyte1_e32 v86, v30
	v_cvt_f32_ubyte2_e32 v87, v30
	v_cvt_f32_ubyte3_e32 v88, v30
	v_fmac_f32_e32 v10, v85, v54
	v_fmac_f32_e32 v11, v86, v54
	v_fmac_f32_e32 v12, v87, v54
	v_fmac_f32_e32 v13, v88, v54
	v_cvt_f32_ubyte0_e32 v85, v31
	v_cvt_f32_ubyte1_e32 v86, v31
	v_cvt_f32_ubyte2_e32 v87, v31
	v_cvt_f32_ubyte3_e32 v88, v31
	v_fmac_f32_e32 v14, v85, v54
	v_fmac_f32_e32 v15, v86, v54
	v_fmac_f32_e32 v16, v87, v54
	v_fmac_f32_e32 v17, v88, v54
	v_and_b32_e32 v84, 0xffff, v80
	v_lshlrev_b32_e32 v109, 1, v84
	v_lshl_or_b32 v83, v84, 7, v89
	global_load_ushort v54, v109, s[14:15]
	global_load_dwordx4 v[28:31], v83, s[12:13]
	s_waitcnt vmcnt(6)
	v_cvt_f32_f16_e32 v55, v55
	v_cvt_f32_ubyte0_e32 v85, v32
	v_cvt_f32_ubyte1_e32 v86, v32
	v_cvt_f32_ubyte2_e32 v87, v32
	v_cvt_f32_ubyte3_e32 v88, v32
	v_fmac_f32_e32 v2, v85, v55
	v_fmac_f32_e32 v3, v86, v55
	v_fmac_f32_e32 v4, v87, v55
	v_fmac_f32_e32 v5, v88, v55
	v_cvt_f32_ubyte0_e32 v85, v33
	v_cvt_f32_ubyte1_e32 v86, v33
	v_cvt_f32_ubyte2_e32 v87, v33
	v_cvt_f32_ubyte3_e32 v88, v33
	v_fmac_f32_e32 v6, v85, v55
	v_fmac_f32_e32 v7, v86, v55
	v_fmac_f32_e32 v8, v87, v55
	v_fmac_f32_e32 v9, v88, v55
	v_cvt_f32_ubyte0_e32 v85, v34
	v_cvt_f32_ubyte1_e32 v86, v34
	v_cvt_f32_ubyte2_e32 v87, v34
	v_cvt_f32_ubyte3_e32 v88, v34
	v_fmac_f32_e32 v10, v85, v55
	v_fmac_f32_e32 v11, v86, v55
	v_fmac_f32_e32 v12, v87, v55
	v_fmac_f32_e32 v13, v88, v55
	v_cvt_f32_ubyte0_e32 v85, v35
	v_cvt_f32_ubyte1_e32 v86, v35
	v_cvt_f32_ubyte2_e32 v87, v35
	v_cvt_f32_ubyte3_e32 v88, v35
	v_fmac_f32_e32 v14, v85, v55
	v_fmac_f32_e32 v15, v86, v55
	v_fmac_f32_e32 v16, v87, v55
	v_fmac_f32_e32 v17, v88, v55
	v_lshrrev_b32_e32 v84, 16, v80
	v_lshlrev_b32_e32 v109, 1, v84
	v_lshl_or_b32 v83, v84, 7, v89
	global_load_ushort v55, v109, s[14:15]
	global_load_dwordx4 v[32:35], v83, s[12:13]
	s_cmp_le_u32 s40, 16
	s_cbranch_scc1 .Lg2_tail0
	s_waitcnt lgkmcnt(0)
	ds_bpermute_b32 v80, v90, v74 offset:4
	s_waitcnt vmcnt(6)
	v_cvt_f32_f16_e32 v52, v52
	v_cvt_f32_ubyte0_e32 v85, v20
	v_cvt_f32_ubyte1_e32 v86, v20
	v_cvt_f32_ubyte2_e32 v87, v20
	v_cvt_f32_ubyte3_e32 v88, v20
	v_fmac_f32_e32 v2, v85, v52
	v_fmac_f32_e32 v3, v86, v52
	v_fmac_f32_e32 v4, v87, v52
	v_fmac_f32_e32 v5, v88, v52
	v_cvt_f32_ubyte0_e32 v85, v21
	v_cvt_f32_ubyte1_e32 v86, v21
	v_cvt_f32_ubyte2_e32 v87, v21
	v_cvt_f32_ubyte3_e32 v88, v21
	v_fmac_f32_e32 v6, v85, v52
	v_fmac_f32_e32 v7, v86, v52
	v_fmac_f32_e32 v8, v87, v52
	v_fmac_f32_e32 v9, v88, v52
	v_cvt_f32_ubyte0_e32 v85, v22
	v_cvt_f32_ubyte1_e32 v86, v22
	v_cvt_f32_ubyte2_e32 v87, v22
	v_cvt_f32_ubyte3_e32 v88, v22
	v_fmac_f32_e32 v10, v85, v52
	v_fmac_f32_e32 v11, v86, v52
	v_fmac_f32_e32 v12, v87, v52
	v_fmac_f32_e32 v13, v88, v52
	v_cvt_f32_ubyte0_e32 v85, v23
	v_cvt_f32_ubyte1_e32 v86, v23
	v_cvt_f32_ubyte2_e32 v87, v23
	v_cvt_f32_ubyte3_e32 v88, v23
	v_fmac_f32_e32 v14, v85, v52
	v_fmac_f32_e32 v15, v86, v52
	v_fmac_f32_e32 v16, v87, v52
	v_fmac_f32_e32 v17, v88, v52
	v_and_b32_e32 v84, 0xffff, v79
	v_lshlrev_b32_e32 v109, 1, v84
	v_lshl_or_b32 v83, v84, 7, v89
	global_load_ushort v52, v109, s[14:15]
	global_load_dwordx4 v[20:23], v83, s[12:13]
	s_waitcnt vmcnt(6)
	v_cvt_f32_f16_e32 v53, v53
	v_cvt_f32_ubyte0_e32 v85, v24
	v_cvt_f32_ubyte1_e32 v86, v24
	v_cvt_f32_ubyte2_e32 v87, v24
	v_cvt_f32_ubyte3_e32 v88, v24
	v_fmac_f32_e32 v2, v85, v53
	v_fmac_f32_e32 v3, v86, v53
	v_fmac_f32_e32 v4, v87, v53
	v_fmac_f32_e32 v5, v88, v53
	v_cvt_f32_ubyte0_e32 v85, v25
	v_cvt_f32_ubyte1_e32 v86, v25
	v_cvt_f32_ubyte2_e32 v87, v25
	v_cvt_f32_ubyte3_e32 v88, v25
	v_fmac_f32_e32 v6, v85, v53
	v_fmac_f32_e32 v7, v86, v53
	v_fmac_f32_e32 v8, v87, v53
	v_fmac_f32_e32 v9, v88, v53
	v_cvt_f32_ubyte0_e32 v85, v26
	v_cvt_f32_ubyte1_e32 v86, v26
	v_cvt_f32_ubyte2_e32 v87, v26
	v_cvt_f32_ubyte3_e32 v88, v26
	v_fmac_f32_e32 v10, v85, v53
	v_fmac_f32_e32 v11, v86, v53
	v_fmac_f32_e32 v12, v87, v53
	v_fmac_f32_e32 v13, v88, v53
	v_cvt_f32_ubyte0_e32 v85, v27
	v_cvt_f32_ubyte1_e32 v86, v27
	v_cvt_f32_ubyte2_e32 v87, v27
	v_cvt_f32_ubyte3_e32 v88, v27
	v_fmac_f32_e32 v14, v85, v53
	v_fmac_f32_e32 v15, v86, v53
	v_fmac_f32_e32 v16, v87, v53
	v_fmac_f32_e32 v17, v88, v53
	v_lshrrev_b32_e32 v84, 16, v79
	v_lshlrev_b32_e32 v109, 1, v84
	v_lshl_or_b32 v83, v84, 7, v89
	global_load_ushort v53, v109, s[14:15]
	global_load_dwordx4 v[24:27], v83, s[12:13]
	s_cmp_le_u32 s40, 18
	s_cbranch_scc1 .Lg2_tail2
	s_waitcnt lgkmcnt(0)
	ds_bpermute_b32 v79, v90, v74 offset:8
	s_waitcnt vmcnt(6)
	v_cvt_f32_f16_e32 v54, v54
	v_cvt_f32_ubyte0_e32 v85, v28
	v_cvt_f32_ubyte1_e32 v86, v28
	v_cvt_f32_ubyte2_e32 v87, v28
	v_cvt_f32_ubyte3_e32 v88, v28
	v_fmac_f32_e32 v2, v85, v54
	v_fmac_f32_e32 v3, v86, v54
	v_fmac_f32_e32 v4, v87, v54
	v_fmac_f32_e32 v5, v88, v54
	v_cvt_f32_ubyte0_e32 v85, v29
	v_cvt_f32_ubyte1_e32 v86, v29
	v_cvt_f32_ubyte2_e32 v87, v29
	v_cvt_f32_ubyte3_e32 v88, v29
	v_fmac_f32_e32 v6, v85, v54
	v_fmac_f32_e32 v7, v86, v54
	v_fmac_f32_e32 v8, v87, v54
	v_fmac_f32_e32 v9, v88, v54
	v_cvt_f32_ubyte0_e32 v85, v30
	v_cvt_f32_ubyte1_e32 v86, v30
	v_cvt_f32_ubyte2_e32 v87, v30
	v_cvt_f32_ubyte3_e32 v88, v30
	v_fmac_f32_e32 v10, v85, v54
	v_fmac_f32_e32 v11, v86, v54
	v_fmac_f32_e32 v12, v87, v54
	v_fmac_f32_e32 v13, v88, v54
	v_cvt_f32_ubyte0_e32 v85, v31
	v_cvt_f32_ubyte1_e32 v86, v31
	v_cvt_f32_ubyte2_e32 v87, v31
	v_cvt_f32_ubyte3_e32 v88, v31
	v_fmac_f32_e32 v14, v85, v54
	v_fmac_f32_e32 v15, v86, v54
	v_fmac_f32_e32 v16, v87, v54
	v_fmac_f32_e32 v17, v88, v54
	v_and_b32_e32 v84, 0xffff, v80
	v_lshlrev_b32_e32 v109, 1, v84
	v_lshl_or_b32 v83, v84, 7, v89
	global_load_ushort v54, v109, s[14:15]
	global_load_dwordx4 v[28:31], v83, s[12:13]
	s_waitcnt vmcnt(6)
	v_cvt_f32_f16_e32 v55, v55
	v_cvt_f32_ubyte0_e32 v85, v32
	v_cvt_f32_ubyte1_e32 v86, v32
	v_cvt_f32_ubyte2_e32 v87, v32
	v_cvt_f32_ubyte3_e32 v88, v32
	v_fmac_f32_e32 v2, v85, v55
	v_fmac_f32_e32 v3, v86, v55
	v_fmac_f32_e32 v4, v87, v55
	v_fmac_f32_e32 v5, v88, v55
	v_cvt_f32_ubyte0_e32 v85, v33
	v_cvt_f32_ubyte1_e32 v86, v33
	v_cvt_f32_ubyte2_e32 v87, v33
	v_cvt_f32_ubyte3_e32 v88, v33
	v_fmac_f32_e32 v6, v85, v55
	v_fmac_f32_e32 v7, v86, v55
	v_fmac_f32_e32 v8, v87, v55
	v_fmac_f32_e32 v9, v88, v55
	v_cvt_f32_ubyte0_e32 v85, v34
	v_cvt_f32_ubyte1_e32 v86, v34
	v_cvt_f32_ubyte2_e32 v87, v34
	v_cvt_f32_ubyte3_e32 v88, v34
	v_fmac_f32_e32 v10, v85, v55
	v_fmac_f32_e32 v11, v86, v55
	v_fmac_f32_e32 v12, v87, v55
	v_fmac_f32_e32 v13, v88, v55
	v_cvt_f32_ubyte0_e32 v85, v35
	v_cvt_f32_ubyte1_e32 v86, v35
	v_cvt_f32_ubyte2_e32 v87, v35
	v_cvt_f32_ubyte3_e32 v88, v35
	v_fmac_f32_e32 v14, v85, v55
	v_fmac_f32_e32 v15, v86, v55
	v_fmac_f32_e32 v16, v87, v55
	v_fmac_f32_e32 v17, v88, v55
	v_lshrrev_b32_e32 v84, 16, v80
	v_lshlrev_b32_e32 v109, 1, v84
	v_lshl_or_b32 v83, v84, 7, v89
	global_load_ushort v55, v109, s[14:15]
	global_load_dwordx4 v[32:35], v83, s[12:13]
	s_cmp_le_u32 s40, 20
	s_cbranch_scc1 .Lg2_tail0
	s_waitcnt lgkmcnt(0)
	ds_bpermute_b32 v80, v90, v74 offset:12
	s_waitcnt vmcnt(6)
	v_cvt_f32_f16_e32 v52, v52
	v_cvt_f32_ubyte0_e32 v85, v20
	v_cvt_f32_ubyte1_e32 v86, v20
	v_cvt_f32_ubyte2_e32 v87, v20
	v_cvt_f32_ubyte3_e32 v88, v20
	v_fmac_f32_e32 v2, v85, v52
	v_fmac_f32_e32 v3, v86, v52
	v_fmac_f32_e32 v4, v87, v52
	v_fmac_f32_e32 v5, v88, v52
	v_cvt_f32_ubyte0_e32 v85, v21
	v_cvt_f32_ubyte1_e32 v86, v21
	v_cvt_f32_ubyte2_e32 v87, v21
	v_cvt_f32_ubyte3_e32 v88, v21
	v_fmac_f32_e32 v6, v85, v52
	v_fmac_f32_e32 v7, v86, v52
	v_fmac_f32_e32 v8, v87, v52
	v_fmac_f32_e32 v9, v88, v52
	v_cvt_f32_ubyte0_e32 v85, v22
	v_cvt_f32_ubyte1_e32 v86, v22
	v_cvt_f32_ubyte2_e32 v87, v22
	v_cvt_f32_ubyte3_e32 v88, v22
	v_fmac_f32_e32 v10, v85, v52
	v_fmac_f32_e32 v11, v86, v52
	v_fmac_f32_e32 v12, v87, v52
	v_fmac_f32_e32 v13, v88, v52
	v_cvt_f32_ubyte0_e32 v85, v23
	v_cvt_f32_ubyte1_e32 v86, v23
	v_cvt_f32_ubyte2_e32 v87, v23
	v_cvt_f32_ubyte3_e32 v88, v23
	v_fmac_f32_e32 v14, v85, v52
	v_fmac_f32_e32 v15, v86, v52
	v_fmac_f32_e32 v16, v87, v52
	v_fmac_f32_e32 v17, v88, v52
	v_and_b32_e32 v84, 0xffff, v79
	v_lshlrev_b32_e32 v109, 1, v84
	v_lshl_or_b32 v83, v84, 7, v89
	global_load_ushort v52, v109, s[14:15]
	global_load_dwordx4 v[20:23], v83, s[12:13]
	s_waitcnt vmcnt(6)
	v_cvt_f32_f16_e32 v53, v53
	v_cvt_f32_ubyte0_e32 v85, v24
	v_cvt_f32_ubyte1_e32 v86, v24
	v_cvt_f32_ubyte2_e32 v87, v24
	v_cvt_f32_ubyte3_e32 v88, v24
	v_fmac_f32_e32 v2, v85, v53
	v_fmac_f32_e32 v3, v86, v53
	v_fmac_f32_e32 v4, v87, v53
	v_fmac_f32_e32 v5, v88, v53
	v_cvt_f32_ubyte0_e32 v85, v25
	v_cvt_f32_ubyte1_e32 v86, v25
	v_cvt_f32_ubyte2_e32 v87, v25
	v_cvt_f32_ubyte3_e32 v88, v25
	v_fmac_f32_e32 v6, v85, v53
	v_fmac_f32_e32 v7, v86, v53
	v_fmac_f32_e32 v8, v87, v53
	v_fmac_f32_e32 v9, v88, v53
	v_cvt_f32_ubyte0_e32 v85, v26
	v_cvt_f32_ubyte1_e32 v86, v26
	v_cvt_f32_ubyte2_e32 v87, v26
	v_cvt_f32_ubyte3_e32 v88, v26
	v_fmac_f32_e32 v10, v85, v53
	v_fmac_f32_e32 v11, v86, v53
	v_fmac_f32_e32 v12, v87, v53
	v_fmac_f32_e32 v13, v88, v53
	v_cvt_f32_ubyte0_e32 v85, v27
	v_cvt_f32_ubyte1_e32 v86, v27
	v_cvt_f32_ubyte2_e32 v87, v27
	v_cvt_f32_ubyte3_e32 v88, v27
	v_fmac_f32_e32 v14, v85, v53
	v_fmac_f32_e32 v15, v86, v53
	v_fmac_f32_e32 v16, v87, v53
	v_fmac_f32_e32 v17, v88, v53
	v_lshrrev_b32_e32 v84, 16, v79
	v_lshlrev_b32_e32 v109, 1, v84
	v_lshl_or_b32 v83, v84, 7, v89
	global_load_ushort v53, v109, s[14:15]
	global_load_dwordx4 v[24:27], v83, s[12:13]
	s_cmp_le_u32 s40, 22
	s_cbranch_scc1 .Lg2_tail2
	s_waitcnt lgkmcnt(0)
	ds_bpermute_b32 v79, v90, v74 offset:16
	s_waitcnt vmcnt(6)
	v_cvt_f32_f16_e32 v54, v54
	v_cvt_f32_ubyte0_e32 v85, v28
	v_cvt_f32_ubyte1_e32 v86, v28
	v_cvt_f32_ubyte2_e32 v87, v28
	v_cvt_f32_ubyte3_e32 v88, v28
	v_fmac_f32_e32 v2, v85, v54
	v_fmac_f32_e32 v3, v86, v54
	v_fmac_f32_e32 v4, v87, v54
	v_fmac_f32_e32 v5, v88, v54
	v_cvt_f32_ubyte0_e32 v85, v29
	v_cvt_f32_ubyte1_e32 v86, v29
	v_cvt_f32_ubyte2_e32 v87, v29
	v_cvt_f32_ubyte3_e32 v88, v29
	v_fmac_f32_e32 v6, v85, v54
	v_fmac_f32_e32 v7, v86, v54
	v_fmac_f32_e32 v8, v87, v54
	v_fmac_f32_e32 v9, v88, v54
	v_cvt_f32_ubyte0_e32 v85, v30
	v_cvt_f32_ubyte1_e32 v86, v30
	v_cvt_f32_ubyte2_e32 v87, v30
	v_cvt_f32_ubyte3_e32 v88, v30
	v_fmac_f32_e32 v10, v85, v54
	v_fmac_f32_e32 v11, v86, v54
	v_fmac_f32_e32 v12, v87, v54
	v_fmac_f32_e32 v13, v88, v54
	v_cvt_f32_ubyte0_e32 v85, v31
	v_cvt_f32_ubyte1_e32 v86, v31
	v_cvt_f32_ubyte2_e32 v87, v31
	v_cvt_f32_ubyte3_e32 v88, v31
	v_fmac_f32_e32 v14, v85, v54
	v_fmac_f32_e32 v15, v86, v54
	v_fmac_f32_e32 v16, v87, v54
	v_fmac_f32_e32 v17, v88, v54
	v_and_b32_e32 v84, 0xffff, v80
	v_lshlrev_b32_e32 v109, 1, v84
	v_lshl_or_b32 v83, v84, 7, v89
	global_load_ushort v54, v109, s[14:15]
	global_load_dwordx4 v[28:31], v83, s[12:13]
	s_waitcnt vmcnt(6)
	v_cvt_f32_f16_e32 v55, v55
	v_cvt_f32_ubyte0_e32 v85, v32
	v_cvt_f32_ubyte1_e32 v86, v32
	v_cvt_f32_ubyte2_e32 v87, v32
	v_cvt_f32_ubyte3_e32 v88, v32
	v_fmac_f32_e32 v2, v85, v55
	v_fmac_f32_e32 v3, v86, v55
	v_fmac_f32_e32 v4, v87, v55
	v_fmac_f32_e32 v5, v88, v55
	v_cvt_f32_ubyte0_e32 v85, v33
	v_cvt_f32_ubyte1_e32 v86, v33
	v_cvt_f32_ubyte2_e32 v87, v33
	v_cvt_f32_ubyte3_e32 v88, v33
	v_fmac_f32_e32 v6, v85, v55
	v_fmac_f32_e32 v7, v86, v55
	v_fmac_f32_e32 v8, v87, v55
	v_fmac_f32_e32 v9, v88, v55
	v_cvt_f32_ubyte0_e32 v85, v34
	v_cvt_f32_ubyte1_e32 v86, v34
	v_cvt_f32_ubyte2_e32 v87, v34
	v_cvt_f32_ubyte3_e32 v88, v34
	v_fmac_f32_e32 v10, v85, v55
	v_fmac_f32_e32 v11, v86, v55
	v_fmac_f32_e32 v12, v87, v55
	v_fmac_f32_e32 v13, v88, v55
	v_cvt_f32_ubyte0_e32 v85, v35
	v_cvt_f32_ubyte1_e32 v86, v35
	v_cvt_f32_ubyte2_e32 v87, v35
	v_cvt_f32_ubyte3_e32 v88, v35
	v_fmac_f32_e32 v14, v85, v55
	v_fmac_f32_e32 v15, v86, v55
	v_fmac_f32_e32 v16, v87, v55
	v_fmac_f32_e32 v17, v88, v55
	v_lshrrev_b32_e32 v84, 16, v80
	v_lshlrev_b32_e32 v109, 1, v84
	v_lshl_or_b32 v83, v84, 7, v89
	global_load_ushort v55, v109, s[14:15]
	global_load_dwordx4 v[32:35], v83, s[12:13]
	s_cmp_le_u32 s40, 24
	s_cbranch_scc1 .Lg2_tail0
	s_waitcnt lgkmcnt(0)
	ds_bpermute_b32 v80, v90, v74 offset:20
	s_waitcnt vmcnt(6)
	v_cvt_f32_f16_e32 v52, v52
	v_cvt_f32_ubyte0_e32 v85, v20
	v_cvt_f32_ubyte1_e32 v86, v20
	v_cvt_f32_ubyte2_e32 v87, v20
	v_cvt_f32_ubyte3_e32 v88, v20
	v_fmac_f32_e32 v2, v85, v52
	v_fmac_f32_e32 v3, v86, v52
	v_fmac_f32_e32 v4, v87, v52
	v_fmac_f32_e32 v5, v88, v52
	v_cvt_f32_ubyte0_e32 v85, v21
	v_cvt_f32_ubyte1_e32 v86, v21
	v_cvt_f32_ubyte2_e32 v87, v21
	v_cvt_f32_ubyte3_e32 v88, v21
	v_fmac_f32_e32 v6, v85, v52
	v_fmac_f32_e32 v7, v86, v52
	v_fmac_f32_e32 v8, v87, v52
	v_fmac_f32_e32 v9, v88, v52
	v_cvt_f32_ubyte0_e32 v85, v22
	v_cvt_f32_ubyte1_e32 v86, v22
	v_cvt_f32_ubyte2_e32 v87, v22
	v_cvt_f32_ubyte3_e32 v88, v22
	v_fmac_f32_e32 v10, v85, v52
	v_fmac_f32_e32 v11, v86, v52
	v_fmac_f32_e32 v12, v87, v52
	v_fmac_f32_e32 v13, v88, v52
	v_cvt_f32_ubyte0_e32 v85, v23
	v_cvt_f32_ubyte1_e32 v86, v23
	v_cvt_f32_ubyte2_e32 v87, v23
	v_cvt_f32_ubyte3_e32 v88, v23
	v_fmac_f32_e32 v14, v85, v52
	v_fmac_f32_e32 v15, v86, v52
	v_fmac_f32_e32 v16, v87, v52
	v_fmac_f32_e32 v17, v88, v52
	v_and_b32_e32 v84, 0xffff, v79
	v_lshlrev_b32_e32 v109, 1, v84
	v_lshl_or_b32 v83, v84, 7, v89
	global_load_ushort v52, v109, s[14:15]
	global_load_dwordx4 v[20:23], v83, s[12:13]
	s_waitcnt vmcnt(6)
	v_cvt_f32_f16_e32 v53, v53
	v_cvt_f32_ubyte0_e32 v85, v24
	v_cvt_f32_ubyte1_e32 v86, v24
	v_cvt_f32_ubyte2_e32 v87, v24
	v_cvt_f32_ubyte3_e32 v88, v24
	v_fmac_f32_e32 v2, v85, v53
	v_fmac_f32_e32 v3, v86, v53
	v_fmac_f32_e32 v4, v87, v53
	v_fmac_f32_e32 v5, v88, v53
	v_cvt_f32_ubyte0_e32 v85, v25
	v_cvt_f32_ubyte1_e32 v86, v25
	v_cvt_f32_ubyte2_e32 v87, v25
	v_cvt_f32_ubyte3_e32 v88, v25
	v_fmac_f32_e32 v6, v85, v53
	v_fmac_f32_e32 v7, v86, v53
	v_fmac_f32_e32 v8, v87, v53
	v_fmac_f32_e32 v9, v88, v53
	v_cvt_f32_ubyte0_e32 v85, v26
	v_cvt_f32_ubyte1_e32 v86, v26
	v_cvt_f32_ubyte2_e32 v87, v26
	v_cvt_f32_ubyte3_e32 v88, v26
	v_fmac_f32_e32 v10, v85, v53
	v_fmac_f32_e32 v11, v86, v53
	v_fmac_f32_e32 v12, v87, v53
	v_fmac_f32_e32 v13, v88, v53
	v_cvt_f32_ubyte0_e32 v85, v27
	v_cvt_f32_ubyte1_e32 v86, v27
	v_cvt_f32_ubyte2_e32 v87, v27
	v_cvt_f32_ubyte3_e32 v88, v27
	v_fmac_f32_e32 v14, v85, v53
	v_fmac_f32_e32 v15, v86, v53
	v_fmac_f32_e32 v16, v87, v53
	v_fmac_f32_e32 v17, v88, v53
	v_lshrrev_b32_e32 v84, 16, v79
	v_lshlrev_b32_e32 v109, 1, v84
	v_lshl_or_b32 v83, v84, 7, v89
	global_load_ushort v53, v109, s[14:15]
	global_load_dwordx4 v[24:27], v83, s[12:13]
	s_cmp_le_u32 s40, 26
	s_cbranch_scc1 .Lg2_tail2
	s_waitcnt lgkmcnt(0)
	ds_bpermute_b32 v79, v90, v74 offset:24
	s_waitcnt vmcnt(6)
	v_cvt_f32_f16_e32 v54, v54
	v_cvt_f32_ubyte0_e32 v85, v28
	v_cvt_f32_ubyte1_e32 v86, v28
	v_cvt_f32_ubyte2_e32 v87, v28
	v_cvt_f32_ubyte3_e32 v88, v28
	v_fmac_f32_e32 v2, v85, v54
	v_fmac_f32_e32 v3, v86, v54
	v_fmac_f32_e32 v4, v87, v54
	v_fmac_f32_e32 v5, v88, v54
	v_cvt_f32_ubyte0_e32 v85, v29
	v_cvt_f32_ubyte1_e32 v86, v29
	v_cvt_f32_ubyte2_e32 v87, v29
	v_cvt_f32_ubyte3_e32 v88, v29
	v_fmac_f32_e32 v6, v85, v54
	v_fmac_f32_e32 v7, v86, v54
	v_fmac_f32_e32 v8, v87, v54
	v_fmac_f32_e32 v9, v88, v54
	v_cvt_f32_ubyte0_e32 v85, v30
	v_cvt_f32_ubyte1_e32 v86, v30
	v_cvt_f32_ubyte2_e32 v87, v30
	v_cvt_f32_ubyte3_e32 v88, v30
	v_fmac_f32_e32 v10, v85, v54
	v_fmac_f32_e32 v11, v86, v54
	v_fmac_f32_e32 v12, v87, v54
	v_fmac_f32_e32 v13, v88, v54
	v_cvt_f32_ubyte0_e32 v85, v31
	v_cvt_f32_ubyte1_e32 v86, v31
	v_cvt_f32_ubyte2_e32 v87, v31
	v_cvt_f32_ubyte3_e32 v88, v31
	v_fmac_f32_e32 v14, v85, v54
	v_fmac_f32_e32 v15, v86, v54
	v_fmac_f32_e32 v16, v87, v54
	v_fmac_f32_e32 v17, v88, v54
	v_and_b32_e32 v84, 0xffff, v80
	v_lshlrev_b32_e32 v109, 1, v84
	v_lshl_or_b32 v83, v84, 7, v89
	global_load_ushort v54, v109, s[14:15]
	global_load_dwordx4 v[28:31], v83, s[12:13]
	s_waitcnt vmcnt(6)
	v_cvt_f32_f16_e32 v55, v55
	v_cvt_f32_ubyte0_e32 v85, v32
	v_cvt_f32_ubyte1_e32 v86, v32
	v_cvt_f32_ubyte2_e32 v87, v32
	v_cvt_f32_ubyte3_e32 v88, v32
	v_fmac_f32_e32 v2, v85, v55
	v_fmac_f32_e32 v3, v86, v55
	v_fmac_f32_e32 v4, v87, v55
	v_fmac_f32_e32 v5, v88, v55
	v_cvt_f32_ubyte0_e32 v85, v33
	v_cvt_f32_ubyte1_e32 v86, v33
	v_cvt_f32_ubyte2_e32 v87, v33
	v_cvt_f32_ubyte3_e32 v88, v33
	v_fmac_f32_e32 v6, v85, v55
	v_fmac_f32_e32 v7, v86, v55
	v_fmac_f32_e32 v8, v87, v55
	v_fmac_f32_e32 v9, v88, v55
	v_cvt_f32_ubyte0_e32 v85, v34
	v_cvt_f32_ubyte1_e32 v86, v34
	v_cvt_f32_ubyte2_e32 v87, v34
	v_cvt_f32_ubyte3_e32 v88, v34
	v_fmac_f32_e32 v10, v85, v55
	v_fmac_f32_e32 v11, v86, v55
	v_fmac_f32_e32 v12, v87, v55
	v_fmac_f32_e32 v13, v88, v55
	v_cvt_f32_ubyte0_e32 v85, v35
	v_cvt_f32_ubyte1_e32 v86, v35
	v_cvt_f32_ubyte2_e32 v87, v35
	v_cvt_f32_ubyte3_e32 v88, v35
	v_fmac_f32_e32 v14, v85, v55
	v_fmac_f32_e32 v15, v86, v55
	v_fmac_f32_e32 v16, v87, v55
	v_fmac_f32_e32 v17, v88, v55
	v_lshrrev_b32_e32 v84, 16, v80
	v_lshlrev_b32_e32 v109, 1, v84
	v_lshl_or_b32 v83, v84, 7, v89
	global_load_ushort v55, v109, s[14:15]
	global_load_dwordx4 v[32:35], v83, s[12:13]
	s_cmp_le_u32 s40, 28
	s_cbranch_scc1 .Lg2_tail0
	s_waitcnt lgkmcnt(0)
	ds_bpermute_b32 v80, v90, v74 offset:28
	s_waitcnt vmcnt(6)
	v_cvt_f32_f16_e32 v52, v52
	v_cvt_f32_ubyte0_e32 v85, v20
	v_cvt_f32_ubyte1_e32 v86, v20
	v_cvt_f32_ubyte2_e32 v87, v20
	v_cvt_f32_ubyte3_e32 v88, v20
	v_fmac_f32_e32 v2, v85, v52
	v_fmac_f32_e32 v3, v86, v52
	v_fmac_f32_e32 v4, v87, v52
	v_fmac_f32_e32 v5, v88, v52
	v_cvt_f32_ubyte0_e32 v85, v21
	v_cvt_f32_ubyte1_e32 v86, v21
	v_cvt_f32_ubyte2_e32 v87, v21
	v_cvt_f32_ubyte3_e32 v88, v21
	v_fmac_f32_e32 v6, v85, v52
	v_fmac_f32_e32 v7, v86, v52
	v_fmac_f32_e32 v8, v87, v52
	v_fmac_f32_e32 v9, v88, v52
	v_cvt_f32_ubyte0_e32 v85, v22
	v_cvt_f32_ubyte1_e32 v86, v22
	v_cvt_f32_ubyte2_e32 v87, v22
	v_cvt_f32_ubyte3_e32 v88, v22
	v_fmac_f32_e32 v10, v85, v52
	v_fmac_f32_e32 v11, v86, v52
	v_fmac_f32_e32 v12, v87, v52
	v_fmac_f32_e32 v13, v88, v52
	v_cvt_f32_ubyte0_e32 v85, v23
	v_cvt_f32_ubyte1_e32 v86, v23
	v_cvt_f32_ubyte2_e32 v87, v23
	v_cvt_f32_ubyte3_e32 v88, v23
	v_fmac_f32_e32 v14, v85, v52
	v_fmac_f32_e32 v15, v86, v52
	v_fmac_f32_e32 v16, v87, v52
	v_fmac_f32_e32 v17, v88, v52
	v_and_b32_e32 v84, 0xffff, v79
	v_lshlrev_b32_e32 v109, 1, v84
	v_lshl_or_b32 v83, v84, 7, v89
	global_load_ushort v52, v109, s[14:15]
	global_load_dwordx4 v[20:23], v83, s[12:13]
	s_waitcnt vmcnt(6)
	v_cvt_f32_f16_e32 v53, v53
	v_cvt_f32_ubyte0_e32 v85, v24
	v_cvt_f32_ubyte1_e32 v86, v24
	v_cvt_f32_ubyte2_e32 v87, v24
	v_cvt_f32_ubyte3_e32 v88, v24
	v_fmac_f32_e32 v2, v85, v53
	v_fmac_f32_e32 v3, v86, v53
	v_fmac_f32_e32 v4, v87, v53
	v_fmac_f32_e32 v5, v88, v53
	v_cvt_f32_ubyte0_e32 v85, v25
	v_cvt_f32_ubyte1_e32 v86, v25
	v_cvt_f32_ubyte2_e32 v87, v25
	v_cvt_f32_ubyte3_e32 v88, v25
	v_fmac_f32_e32 v6, v85, v53
	v_fmac_f32_e32 v7, v86, v53
	v_fmac_f32_e32 v8, v87, v53
	v_fmac_f32_e32 v9, v88, v53
	v_cvt_f32_ubyte0_e32 v85, v26
	v_cvt_f32_ubyte1_e32 v86, v26
	v_cvt_f32_ubyte2_e32 v87, v26
	v_cvt_f32_ubyte3_e32 v88, v26
	v_fmac_f32_e32 v10, v85, v53
	v_fmac_f32_e32 v11, v86, v53
	v_fmac_f32_e32 v12, v87, v53
	v_fmac_f32_e32 v13, v88, v53
	v_cvt_f32_ubyte0_e32 v85, v27
	v_cvt_f32_ubyte1_e32 v86, v27
	v_cvt_f32_ubyte2_e32 v87, v27
	v_cvt_f32_ubyte3_e32 v88, v27
	v_fmac_f32_e32 v14, v85, v53
	v_fmac_f32_e32 v15, v86, v53
	v_fmac_f32_e32 v16, v87, v53
	v_fmac_f32_e32 v17, v88, v53
	v_lshrrev_b32_e32 v84, 16, v79
	v_lshlrev_b32_e32 v109, 1, v84
	v_lshl_or_b32 v83, v84, 7, v89
	global_load_ushort v53, v109, s[14:15]
	global_load_dwordx4 v[24:27], v83, s[12:13]
	s_cmp_le_u32 s40, 30
	s_cbranch_scc1 .Lg2_tail2
	s_waitcnt lgkmcnt(0)
	s_waitcnt vmcnt(6)
	v_cvt_f32_f16_e32 v54, v54
	v_cvt_f32_ubyte0_e32 v85, v28
	v_cvt_f32_ubyte1_e32 v86, v28
	v_cvt_f32_ubyte2_e32 v87, v28
	v_cvt_f32_ubyte3_e32 v88, v28
	v_fmac_f32_e32 v2, v85, v54
	v_fmac_f32_e32 v3, v86, v54
	v_fmac_f32_e32 v4, v87, v54
	v_fmac_f32_e32 v5, v88, v54
	v_cvt_f32_ubyte0_e32 v85, v29
	v_cvt_f32_ubyte1_e32 v86, v29
	v_cvt_f32_ubyte2_e32 v87, v29
	v_cvt_f32_ubyte3_e32 v88, v29
	v_fmac_f32_e32 v6, v85, v54
	v_fmac_f32_e32 v7, v86, v54
	v_fmac_f32_e32 v8, v87, v54
	v_fmac_f32_e32 v9, v88, v54
	v_cvt_f32_ubyte0_e32 v85, v30
	v_cvt_f32_ubyte1_e32 v86, v30
	v_cvt_f32_ubyte2_e32 v87, v30
	v_cvt_f32_ubyte3_e32 v88, v30
	v_fmac_f32_e32 v10, v85, v54
	v_fmac_f32_e32 v11, v86, v54
	v_fmac_f32_e32 v12, v87, v54
	v_fmac_f32_e32 v13, v88, v54
	v_cvt_f32_ubyte0_e32 v85, v31
	v_cvt_f32_ubyte1_e32 v86, v31
	v_cvt_f32_ubyte2_e32 v87, v31
	v_cvt_f32_ubyte3_e32 v88, v31
	v_fmac_f32_e32 v14, v85, v54
	v_fmac_f32_e32 v15, v86, v54
	v_fmac_f32_e32 v16, v87, v54
	v_fmac_f32_e32 v17, v88, v54
	v_and_b32_e32 v84, 0xffff, v80
	v_lshlrev_b32_e32 v109, 1, v84
	v_lshl_or_b32 v83, v84, 7, v89
	global_load_ushort v54, v109, s[14:15]
	global_load_dwordx4 v[28:31], v83, s[12:13]
	s_waitcnt vmcnt(6)
	v_cvt_f32_f16_e32 v55, v55
	v_cvt_f32_ubyte0_e32 v85, v32
	v_cvt_f32_ubyte1_e32 v86, v32
	v_cvt_f32_ubyte2_e32 v87, v32
	v_cvt_f32_ubyte3_e32 v88, v32
	v_fmac_f32_e32 v2, v85, v55
	v_fmac_f32_e32 v3, v86, v55
	v_fmac_f32_e32 v4, v87, v55
	v_fmac_f32_e32 v5, v88, v55
	v_cvt_f32_ubyte0_e32 v85, v33
	v_cvt_f32_ubyte1_e32 v86, v33
	v_cvt_f32_ubyte2_e32 v87, v33
	v_cvt_f32_ubyte3_e32 v88, v33
	v_fmac_f32_e32 v6, v85, v55
	v_fmac_f32_e32 v7, v86, v55
	v_fmac_f32_e32 v8, v87, v55
	v_fmac_f32_e32 v9, v88, v55
	v_cvt_f32_ubyte0_e32 v85, v34
	v_cvt_f32_ubyte1_e32 v86, v34
	v_cvt_f32_ubyte2_e32 v87, v34
	v_cvt_f32_ubyte3_e32 v88, v34
	v_fmac_f32_e32 v10, v85, v55
	v_fmac_f32_e32 v11, v86, v55
	v_fmac_f32_e32 v12, v87, v55
	v_fmac_f32_e32 v13, v88, v55
	v_cvt_f32_ubyte0_e32 v85, v35
	v_cvt_f32_ubyte1_e32 v86, v35
	v_cvt_f32_ubyte2_e32 v87, v35
	v_cvt_f32_ubyte3_e32 v88, v35
	v_fmac_f32_e32 v14, v85, v55
	v_fmac_f32_e32 v15, v86, v55
	v_fmac_f32_e32 v16, v87, v55
	v_fmac_f32_e32 v17, v88, v55
	v_lshrrev_b32_e32 v84, 16, v80
	v_lshlrev_b32_e32 v109, 1, v84
	v_lshl_or_b32 v83, v84, 7, v89
	global_load_ushort v55, v109, s[14:15]
	global_load_dwordx4 v[32:35], v83, s[12:13]

.Lg2_tail2:
	s_cmp_eq_u32 s39, 1
	s_cbranch_scc1 .Lg2_tailb2
	s_waitcnt vmcnt(6)
	v_cvt_f32_f16_e32 v54, v54
	v_cvt_f32_ubyte0_e32 v85, v28
	v_cvt_f32_ubyte1_e32 v86, v28
	v_cvt_f32_ubyte2_e32 v87, v28
	v_cvt_f32_ubyte3_e32 v88, v28
	v_fmac_f32_e32 v2, v85, v54
	v_fmac_f32_e32 v3, v86, v54
	v_fmac_f32_e32 v4, v87, v54
	v_fmac_f32_e32 v5, v88, v54
	v_cvt_f32_ubyte0_e32 v85, v29
	v_cvt_f32_ubyte1_e32 v86, v29
	v_cvt_f32_ubyte2_e32 v87, v29
	v_cvt_f32_ubyte3_e32 v88, v29
	v_fmac_f32_e32 v6, v85, v54
	v_fmac_f32_e32 v7, v86, v54
	v_fmac_f32_e32 v8, v87, v54
	v_fmac_f32_e32 v9, v88, v54
	v_cvt_f32_ubyte0_e32 v85, v30
	v_cvt_f32_ubyte1_e32 v86, v30
	v_cvt_f32_ubyte2_e32 v87, v30
	v_cvt_f32_ubyte3_e32 v88, v30
	v_fmac_f32_e32 v10, v85, v54
	v_fmac_f32_e32 v11, v86, v54
	v_fmac_f32_e32 v12, v87, v54
	v_fmac_f32_e32 v13, v88, v54
	v_cvt_f32_ubyte0_e32 v85, v31
	v_cvt_f32_ubyte1_e32 v86, v31
	v_cvt_f32_ubyte2_e32 v87, v31
	v_cvt_f32_ubyte3_e32 v88, v31
	v_fmac_f32_e32 v14, v85, v54
	v_fmac_f32_e32 v15, v86, v54
	v_fmac_f32_e32 v16, v87, v54
	v_fmac_f32_e32 v17, v88, v54
	s_waitcnt vmcnt(4)
	v_cvt_f32_f16_e32 v55, v55
	v_cvt_f32_ubyte0_e32 v85, v32
	v_cvt_f32_ubyte1_e32 v86, v32
	v_cvt_f32_ubyte2_e32 v87, v32
	v_cvt_f32_ubyte3_e32 v88, v32
	v_fmac_f32_e32 v2, v85, v55
	v_fmac_f32_e32 v3, v86, v55
	v_fmac_f32_e32 v4, v87, v55
	v_fmac_f32_e32 v5, v88, v55
	v_cvt_f32_ubyte0_e32 v85, v33
	v_cvt_f32_ubyte1_e32 v86, v33
	v_cvt_f32_ubyte2_e32 v87, v33
	v_cvt_f32_ubyte3_e32 v88, v33
	v_fmac_f32_e32 v6, v85, v55
	v_fmac_f32_e32 v7, v86, v55
	v_fmac_f32_e32 v8, v87, v55
	v_fmac_f32_e32 v9, v88, v55
	v_cvt_f32_ubyte0_e32 v85, v34
	v_cvt_f32_ubyte1_e32 v86, v34
	v_cvt_f32_ubyte2_e32 v87, v34
	v_cvt_f32_ubyte3_e32 v88, v34
	v_fmac_f32_e32 v10, v85, v55
	v_fmac_f32_e32 v11, v86, v55
	v_fmac_f32_e32 v12, v87, v55
	v_fmac_f32_e32 v13, v88, v55
	v_cvt_f32_ubyte0_e32 v85, v35
	v_cvt_f32_ubyte1_e32 v86, v35
	v_cvt_f32_ubyte2_e32 v87, v35
	v_cvt_f32_ubyte3_e32 v88, v35
	v_fmac_f32_e32 v14, v85, v55
	v_fmac_f32_e32 v15, v86, v55
	v_fmac_f32_e32 v16, v87, v55
	v_fmac_f32_e32 v17, v88, v55
	s_waitcnt vmcnt(2)
	v_cvt_f32_f16_e32 v52, v52
	v_cvt_f32_ubyte0_e32 v85, v20
	v_cvt_f32_ubyte1_e32 v86, v20
	v_cvt_f32_ubyte2_e32 v87, v20
	v_cvt_f32_ubyte3_e32 v88, v20
	v_fmac_f32_e32 v2, v85, v52
	v_fmac_f32_e32 v3, v86, v52
	v_fmac_f32_e32 v4, v87, v52
	v_fmac_f32_e32 v5, v88, v52
	v_cvt_f32_ubyte0_e32 v85, v21
	v_cvt_f32_ubyte1_e32 v86, v21
	v_cvt_f32_ubyte2_e32 v87, v21
	v_cvt_f32_ubyte3_e32 v88, v21
	v_fmac_f32_e32 v6, v85, v52
	v_fmac_f32_e32 v7, v86, v52
	v_fmac_f32_e32 v8, v87, v52
	v_fmac_f32_e32 v9, v88, v52
	v_cvt_f32_ubyte0_e32 v85, v22
	v_cvt_f32_ubyte1_e32 v86, v22
	v_cvt_f32_ubyte2_e32 v87, v22
	v_cvt_f32_ubyte3_e32 v88, v22
	v_fmac_f32_e32 v10, v85, v52
	v_fmac_f32_e32 v11, v86, v52
	v_fmac_f32_e32 v12, v87, v52
	v_fmac_f32_e32 v13, v88, v52
	v_cvt_f32_ubyte0_e32 v85, v23
	v_cvt_f32_ubyte1_e32 v86, v23
	v_cvt_f32_ubyte2_e32 v87, v23
	v_cvt_f32_ubyte3_e32 v88, v23
	v_fmac_f32_e32 v14, v85, v52
	v_fmac_f32_e32 v15, v86, v52
	v_fmac_f32_e32 v16, v87, v52
	v_fmac_f32_e32 v17, v88, v52
	s_waitcnt vmcnt(0)
	v_cvt_f32_f16_e32 v53, v53
	v_cvt_f32_ubyte0_e32 v85, v24
	v_cvt_f32_ubyte1_e32 v86, v24
	v_cvt_f32_ubyte2_e32 v87, v24
	v_cvt_f32_ubyte3_e32 v88, v24
	v_fmac_f32_e32 v2, v85, v53
	v_fmac_f32_e32 v3, v86, v53
	v_fmac_f32_e32 v4, v87, v53
	v_fmac_f32_e32 v5, v88, v53
	v_cvt_f32_ubyte0_e32 v85, v25
	v_cvt_f32_ubyte1_e32 v86, v25
	v_cvt_f32_ubyte2_e32 v87, v25
	v_cvt_f32_ubyte3_e32 v88, v25
	v_fmac_f32_e32 v6, v85, v53
	v_fmac_f32_e32 v7, v86, v53
	v_fmac_f32_e32 v8, v87, v53
	v_fmac_f32_e32 v9, v88, v53
	v_cvt_f32_ubyte0_e32 v85, v26
	v_cvt_f32_ubyte1_e32 v86, v26
	v_cvt_f32_ubyte2_e32 v87, v26
	v_cvt_f32_ubyte3_e32 v88, v26
	v_fmac_f32_e32 v10, v85, v53
	v_fmac_f32_e32 v11, v86, v53
	v_fmac_f32_e32 v12, v87, v53
	v_fmac_f32_e32 v13, v88, v53
	v_cvt_f32_ubyte0_e32 v85, v27
	v_cvt_f32_ubyte1_e32 v86, v27
	v_cvt_f32_ubyte2_e32 v87, v27
	v_cvt_f32_ubyte3_e32 v88, v27
	v_fmac_f32_e32 v14, v85, v53
	v_fmac_f32_e32 v15, v86, v53
	v_fmac_f32_e32 v16, v87, v53
	v_fmac_f32_e32 v17, v88, v53
	s_branch .Lg2_rare_check
.Lg2_tailb2:
	s_waitcnt vmcnt(6)
	v_cvt_f32_f16_e32 v54, v54
	v_cvt_f32_ubyte0_e32 v85, v28
	v_cvt_f32_ubyte1_e32 v86, v28
	v_cvt_f32_ubyte2_e32 v87, v28
	v_cvt_f32_ubyte3_e32 v88, v28
	v_fmac_f32_e32 v2, v85, v54
	v_fmac_f32_e32 v3, v86, v54
	v_fmac_f32_e32 v4, v87, v54
	v_fmac_f32_e32 v5, v88, v54
	v_cvt_f32_ubyte0_e32 v85, v29
	v_cvt_f32_ubyte1_e32 v86, v29
	v_cvt_f32_ubyte2_e32 v87, v29
	v_cvt_f32_ubyte3_e32 v88, v29
	v_fmac_f32_e32 v6, v85, v54
	v_fmac_f32_e32 v7, v86, v54
	v_fmac_f32_e32 v8, v87, v54
	v_fmac_f32_e32 v9, v88, v54
	v_cvt_f32_ubyte0_e32 v85, v30
	v_cvt_f32_ubyte1_e32 v86, v30
	v_cvt_f32_ubyte2_e32 v87, v30
	v_cvt_f32_ubyte3_e32 v88, v30
	v_fmac_f32_e32 v10, v85, v54
	v_fmac_f32_e32 v11, v86, v54
	v_fmac_f32_e32 v12, v87, v54
	v_fmac_f32_e32 v13, v88, v54
	v_cvt_f32_ubyte0_e32 v85, v31
	v_cvt_f32_ubyte1_e32 v86, v31
	v_cvt_f32_ubyte2_e32 v87, v31
	v_cvt_f32_ubyte3_e32 v88, v31
	v_fmac_f32_e32 v14, v85, v54
	v_fmac_f32_e32 v15, v86, v54
	v_fmac_f32_e32 v16, v87, v54
	v_fmac_f32_e32 v17, v88, v54
	global_load_dwordx4 v[112:115], v103, s[10:11] offset:0
	s_waitcnt vmcnt(5)
	v_cvt_f32_f16_e32 v55, v55
	v_cvt_f32_ubyte0_e32 v85, v32
	v_cvt_f32_ubyte1_e32 v86, v32
	v_cvt_f32_ubyte2_e32 v87, v32
	v_cvt_f32_ubyte3_e32 v88, v32
	v_fmac_f32_e32 v2, v85, v55
	v_fmac_f32_e32 v3, v86, v55
	v_fmac_f32_e32 v4, v87, v55
	v_fmac_f32_e32 v5, v88, v55
	v_cvt_f32_ubyte0_e32 v85, v33
	v_cvt_f32_ubyte1_e32 v86, v33
	v_cvt_f32_ubyte2_e32 v87, v33
	v_cvt_f32_ubyte3_e32 v88, v33
	v_fmac_f32_e32 v6, v85, v55
	v_fmac_f32_e32 v7, v86, v55
	v_fmac_f32_e32 v8, v87, v55
	v_fmac_f32_e32 v9, v88, v55
	v_cvt_f32_ubyte0_e32 v85, v34
	v_cvt_f32_ubyte1_e32 v86, v34
	v_cvt_f32_ubyte2_e32 v87, v34
	v_cvt_f32_ubyte3_e32 v88, v34
	v_fmac_f32_e32 v10, v85, v55
	v_fmac_f32_e32 v11, v86, v55
	v_fmac_f32_e32 v12, v87, v55
	v_fmac_f32_e32 v13, v88, v55
	v_cvt_f32_ubyte0_e32 v85, v35
	v_cvt_f32_ubyte1_e32 v86, v35
	v_cvt_f32_ubyte2_e32 v87, v35
	v_cvt_f32_ubyte3_e32 v88, v35
	v_fmac_f32_e32 v14, v85, v55
	v_fmac_f32_e32 v15, v86, v55
	v_fmac_f32_e32 v16, v87, v55
	v_fmac_f32_e32 v17, v88, v55
	global_load_dwordx4 v[116:119], v103, s[10:11] offset:64
	s_waitcnt vmcnt(4)
	v_cvt_f32_f16_e32 v52, v52
	v_cvt_f32_ubyte0_e32 v85, v20
	v_cvt_f32_ubyte1_e32 v86, v20
	v_cvt_f32_ubyte2_e32 v87, v20
	v_cvt_f32_ubyte3_e32 v88, v20
	v_fmac_f32_e32 v2, v85, v52
	v_fmac_f32_e32 v3, v86, v52
	v_fmac_f32_e32 v4, v87, v52
	v_fmac_f32_e32 v5, v88, v52
	v_cvt_f32_ubyte0_e32 v85, v21
	v_cvt_f32_ubyte1_e32 v86, v21
	v_cvt_f32_ubyte2_e32 v87, v21
	v_cvt_f32_ubyte3_e32 v88, v21
	v_fmac_f32_e32 v6, v85, v52
	v_fmac_f32_e32 v7, v86, v52
	v_fmac_f32_e32 v8, v87, v52
	v_fmac_f32_e32 v9, v88, v52
	v_cvt_f32_ubyte0_e32 v85, v22
	v_cvt_f32_ubyte1_e32 v86, v22
	v_cvt_f32_ubyte2_e32 v87, v22
	v_cvt_f32_ubyte3_e32 v88, v22
	v_fmac_f32_e32 v10, v85, v52
	v_fmac_f32_e32 v11, v86, v52
	v_fmac_f32_e32 v12, v87, v52
	v_fmac_f32_e32 v13, v88, v52
	v_cvt_f32_ubyte0_e32 v85, v23
	v_cvt_f32_ubyte1_e32 v86, v23
	v_cvt_f32_ubyte2_e32 v87, v23
	v_cvt_f32_ubyte3_e32 v88, v23
	v_fmac_f32_e32 v14, v85, v52
	v_fmac_f32_e32 v15, v86, v52
	v_fmac_f32_e32 v16, v87, v52
	v_fmac_f32_e32 v17, v88, v52
	global_load_dwordx4 v[120:123], v103, s[10:11] offset:128
	s_waitcnt vmcnt(3)
	v_cvt_f32_f16_e32 v53, v53
	v_cvt_f32_ubyte0_e32 v85, v24
	v_cvt_f32_ubyte1_e32 v86, v24
	v_cvt_f32_ubyte2_e32 v87, v24
	v_cvt_f32_ubyte3_e32 v88, v24
	v_fmac_f32_e32 v2, v85, v53
	v_fmac_f32_e32 v3, v86, v53
	v_fmac_f32_e32 v4, v87, v53
	v_fmac_f32_e32 v5, v88, v53
	v_cvt_f32_ubyte0_e32 v85, v25
	v_cvt_f32_ubyte1_e32 v86, v25
	v_cvt_f32_ubyte2_e32 v87, v25
	v_cvt_f32_ubyte3_e32 v88, v25
	v_fmac_f32_e32 v6, v85, v53
	v_fmac_f32_e32 v7, v86, v53
	v_fmac_f32_e32 v8, v87, v53
	v_fmac_f32_e32 v9, v88, v53
	v_cvt_f32_ubyte0_e32 v85, v26
	v_cvt_f32_ubyte1_e32 v86, v26
	v_cvt_f32_ubyte2_e32 v87, v26
	v_cvt_f32_ubyte3_e32 v88, v26
	v_fmac_f32_e32 v10, v85, v53
	v_fmac_f32_e32 v11, v86, v53
	v_fmac_f32_e32 v12, v87, v53
	v_fmac_f32_e32 v13, v88, v53
	v_cvt_f32_ubyte0_e32 v85, v27
	v_cvt_f32_ubyte1_e32 v86, v27
	v_cvt_f32_ubyte2_e32 v87, v27
	v_cvt_f32_ubyte3_e32 v88, v27
	v_fmac_f32_e32 v14, v85, v53
	v_fmac_f32_e32 v15, v86, v53
	v_fmac_f32_e32 v16, v87, v53
	v_fmac_f32_e32 v17, v88, v53
	global_load_dwordx4 v[124:127], v103, s[10:11] offset:192
	s_branch .Lg2_rare_check
